# epilogues of P5a, P5b, P6 pipelined (rolling row loads in flight), P11 final_g hoisted, P7 u2 pass pipelined
# baseline (speedup 1.0000x reference)
; __device__ __forceinline__ unsigned cvt_pk_bf16(float lo, float hi) { unsigned r; asm volatile("v_cvt_pk_bf16_f32 %0, %1, %2" : "=v"(r) : "v"(lo), "v"(hi)); return r; }
; __device__ __forceinline__ float bf_lo(unsigned w) { return __uint_as_float(w << 16); }
; __device__ __forceinline__ float bf_hi(unsigned w) { return __uint_as_float(w & 0xffff0000u); }
;     __device__ __forceinline__ void operator()(const f32x4 (&acc)[2][2][4][2], const Unit& u, int wr, int wc, int fr, int fq) const {
;         const int row0 = u.pm * BM + wr * 64 + fr; const int col0 = u.pn * BM + wc * 32 + 8 * fq;
; #pragma unroll
;         for (int ai = 0; ai < 2; ++ai)
; #pragma unroll
;             for (int m = 0; m < 4; ++m) { const size_t row = (size_t)(row0 + ai * HALF + m * 16);
; #pragma unroll
;                 for (int bj = 0; bj < 2; ++bj) { const int col = col0 + bj * HALF; const u32x4 g = *(const u32x4*)(G + row * ldg + col);
;                     const f32x4 a0 = acc[ai][bj][m][0] * P5_ACC_SCALE, a1 = acc[ai][bj][m][1] * P5_ACC_SCALE;
;                     const f32x4 o0 = {a0[0] * bf_lo(g.x), a0[1] * bf_hi(g.x), a0[2] * bf_lo(g.y), a0[3] * bf_hi(g.y)};
;                     const f32x4 o1 = {a1[0] * bf_lo(g.z), a1[1] * bf_hi(g.z), a1[2] * bf_lo(g.w), a1[3] * bf_hi(g.w)};
;                     u32x4 w; w.x = cvt_pk_bf16(o0[0], o0[1]); w.y = cvt_pk_bf16(o0[2], o0[3]); w.z = cvt_pk_bf16(o1[0], o1[1]); w.w = cvt_pk_bf16(o1[2], o1[3]);
;                     *(u32x4*)(M1 + row * 2048 + col) = w; } }
;     }
.LBB0_733:
	v_lshl_or_b32 v2, s69, 8, v193
	v_lshl_add_u32 v4, s58, 8, v191
	v_mov_b64_e32 v[6:7], s[36:37]
	v_ashrrev_i32_e32 v3, 31, v2
	v_mad_i64_i32 v[8:9], s[60:61], v4, s68, v[6:7]
	v_lshlrev_b64 v[2:3], 1, v[2:3]
	v_lshl_add_u64 v[12:13], v[8:9], 0, v[2:3]
	s_andn2_b64 vcc, exec, s[4:5]
	s_mov_b64 s[4:5], -1
	v_add_u32_e32 v32, 0x0, v4
	v_mad_i64_i32 v[254:255], s[82:83], v32, s68, v[6:7]
	v_lshl_add_u64 v[254:255], v[254:255], 0, v[2:3]
	global_load_dwordx4 v[204:207], v[254:255], off
	global_load_dwordx4 v[208:211], v[254:255], off offset:256
	v_add_u32_e32 v32, 0x10, v4
	v_mad_i64_i32 v[254:255], s[82:83], v32, s68, v[6:7]
	v_lshl_add_u64 v[254:255], v[254:255], 0, v[2:3]
	global_load_dwordx4 v[212:215], v[254:255], off
	global_load_dwordx4 v[216:219], v[254:255], off offset:256
	v_add_u32_e32 v32, 0x20, v4
	v_mad_i64_i32 v[254:255], s[82:83], v32, s68, v[6:7]
	v_lshl_add_u64 v[254:255], v[254:255], 0, v[2:3]
	global_load_dwordx4 v[220:223], v[254:255], off
	global_load_dwordx4 v[224:227], v[254:255], off offset:256
	v_add_u32_e32 v32, 0x30, v4
	v_mad_i64_i32 v[254:255], s[82:83], v32, s68, v[6:7]
	v_lshl_add_u64 v[254:255], v[254:255], 0, v[2:3]
	global_load_dwordx4 v[228:231], v[254:255], off
	global_load_dwordx4 v[232:235], v[254:255], off offset:256
	v_add_u32_e32 v33, 0x0, v4
	v_lshlrev_b32_e32 v30, 12, v33
	v_mov_b32_e32 v31, 0
	v_lshl_add_u64 v[30:31], s[8:9], 0, v[30:31]
	v_lshl_add_u64 v[30:31], v[30:31], 0, v[2:3]
	s_waitcnt vmcnt(7)
	v_lshlrev_b32_e32 v236, 16, v204
	v_and_b32_e32 v237, 0xffff0000, v204
	v_lshlrev_b32_e32 v238, 16, v205
	v_and_b32_e32 v239, 0xffff0000, v205
	v_lshlrev_b32_e32 v240, 16, v206
	v_and_b32_e32 v241, 0xffff0000, v206
	v_lshlrev_b32_e32 v242, 16, v207
	v_and_b32_e32 v243, 0xffff0000, v207
	v_pk_mul_f32 v[244:245], v[158:159], s[42:43] op_sel_hi:[1,0]
	v_pk_mul_f32 v[248:249], v[160:161], s[42:43] op_sel_hi:[1,0]
	v_pk_mul_f32 v[250:251], v[154:155], s[42:43] op_sel_hi:[1,0]
	v_pk_mul_f32 v[252:253], v[156:157], s[42:43] op_sel_hi:[1,0]
	v_pk_mul_f32 v[244:245], v[244:245], v[236:237]
	v_pk_mul_f32 v[248:249], v[248:249], v[238:239]
	v_pk_mul_f32 v[250:251], v[250:251], v[240:241]
	v_pk_mul_f32 v[252:253], v[252:253], v[242:243]
	v_cvt_pk_bf16_f32 v204, v244, v245
	v_cvt_pk_bf16_f32 v205, v248, v249
	v_cvt_pk_bf16_f32 v206, v250, v251
	v_cvt_pk_bf16_f32 v207, v252, v253
	global_store_dwordx4 v[30:31], v[204:207], off
	v_add_u32_e32 v32, 0x80, v4
	v_mad_i64_i32 v[254:255], s[82:83], v32, s68, v[6:7]
	v_lshl_add_u64 v[254:255], v[254:255], 0, v[2:3]
	global_load_dwordx4 v[204:207], v[254:255], off
	s_waitcnt vmcnt(8)
	v_lshlrev_b32_e32 v236, 16, v208
	v_and_b32_e32 v237, 0xffff0000, v208
	v_lshlrev_b32_e32 v238, 16, v209
	v_and_b32_e32 v239, 0xffff0000, v209
	v_lshlrev_b32_e32 v240, 16, v210
	v_and_b32_e32 v241, 0xffff0000, v210
	v_lshlrev_b32_e32 v242, 16, v211
	v_and_b32_e32 v243, 0xffff0000, v211
	v_pk_mul_f32 v[244:245], v[150:151], s[42:43] op_sel_hi:[1,0]
	v_pk_mul_f32 v[248:249], v[152:153], s[42:43] op_sel_hi:[1,0]
	v_pk_mul_f32 v[250:251], v[146:147], s[42:43] op_sel_hi:[1,0]
	v_pk_mul_f32 v[252:253], v[148:149], s[42:43] op_sel_hi:[1,0]
	v_pk_mul_f32 v[244:245], v[244:245], v[236:237]
	v_pk_mul_f32 v[248:249], v[248:249], v[238:239]
	v_pk_mul_f32 v[250:251], v[250:251], v[240:241]
	v_pk_mul_f32 v[252:253], v[252:253], v[242:243]
	v_cvt_pk_bf16_f32 v208, v244, v245
	v_cvt_pk_bf16_f32 v209, v248, v249
	v_cvt_pk_bf16_f32 v210, v250, v251
	v_cvt_pk_bf16_f32 v211, v252, v253
	global_store_dwordx4 v[30:31], v[208:211], off offset:256
	global_load_dwordx4 v[208:211], v[254:255], off offset:256
	v_add_u32_e32 v33, 0x10, v4
	v_lshlrev_b32_e32 v30, 12, v33
	v_mov_b32_e32 v31, 0
	v_lshl_add_u64 v[30:31], s[8:9], 0, v[30:31]
	v_lshl_add_u64 v[30:31], v[30:31], 0, v[2:3]
	s_waitcnt vmcnt(9)
	v_lshlrev_b32_e32 v236, 16, v212
	v_and_b32_e32 v237, 0xffff0000, v212
	v_lshlrev_b32_e32 v238, 16, v213
	v_and_b32_e32 v239, 0xffff0000, v213
	v_lshlrev_b32_e32 v240, 16, v214
	v_and_b32_e32 v241, 0xffff0000, v214
	v_lshlrev_b32_e32 v242, 16, v215
	v_and_b32_e32 v243, 0xffff0000, v215
	v_pk_mul_f32 v[244:245], v[142:143], s[42:43] op_sel_hi:[1,0]
	v_pk_mul_f32 v[248:249], v[144:145], s[42:43] op_sel_hi:[1,0]
	v_pk_mul_f32 v[250:251], v[138:139], s[42:43] op_sel_hi:[1,0]
	v_pk_mul_f32 v[252:253], v[140:141], s[42:43] op_sel_hi:[1,0]
	v_pk_mul_f32 v[244:245], v[244:245], v[236:237]
	v_pk_mul_f32 v[248:249], v[248:249], v[238:239]
	v_pk_mul_f32 v[250:251], v[250:251], v[240:241]
	v_pk_mul_f32 v[252:253], v[252:253], v[242:243]
	v_cvt_pk_bf16_f32 v212, v244, v245
	v_cvt_pk_bf16_f32 v213, v248, v249
	v_cvt_pk_bf16_f32 v214, v250, v251
	v_cvt_pk_bf16_f32 v215, v252, v253
	global_store_dwordx4 v[30:31], v[212:215], off
	v_add_u32_e32 v32, 0x90, v4
	v_mad_i64_i32 v[254:255], s[82:83], v32, s68, v[6:7]
	v_lshl_add_u64 v[254:255], v[254:255], 0, v[2:3]
	global_load_dwordx4 v[212:215], v[254:255], off
	s_waitcnt vmcnt(10)
	v_lshlrev_b32_e32 v236, 16, v216
	v_and_b32_e32 v237, 0xffff0000, v216
	v_lshlrev_b32_e32 v238, 16, v217
	v_and_b32_e32 v239, 0xffff0000, v217
	v_lshlrev_b32_e32 v240, 16, v218
	v_and_b32_e32 v241, 0xffff0000, v218
	v_lshlrev_b32_e32 v242, 16, v219
	v_and_b32_e32 v243, 0xffff0000, v219
	v_pk_mul_f32 v[244:245], v[134:135], s[42:43] op_sel_hi:[1,0]
	v_pk_mul_f32 v[248:249], v[136:137], s[42:43] op_sel_hi:[1,0]
	v_pk_mul_f32 v[250:251], v[130:131], s[42:43] op_sel_hi:[1,0]
	v_pk_mul_f32 v[252:253], v[132:133], s[42:43] op_sel_hi:[1,0]
	v_pk_mul_f32 v[244:245], v[244:245], v[236:237]
	v_pk_mul_f32 v[248:249], v[248:249], v[238:239]
	v_pk_mul_f32 v[250:251], v[250:251], v[240:241]
	v_pk_mul_f32 v[252:253], v[252:253], v[242:243]
	v_cvt_pk_bf16_f32 v216, v244, v245
	v_cvt_pk_bf16_f32 v217, v248, v249
	v_cvt_pk_bf16_f32 v218, v250, v251
	v_cvt_pk_bf16_f32 v219, v252, v253
	global_store_dwordx4 v[30:31], v[216:219], off offset:256
	global_load_dwordx4 v[216:219], v[254:255], off offset:256
	v_add_u32_e32 v33, 0x20, v4
	v_lshlrev_b32_e32 v30, 12, v33
	v_mov_b32_e32 v31, 0
	v_lshl_add_u64 v[30:31], s[8:9], 0, v[30:31]
	v_lshl_add_u64 v[30:31], v[30:31], 0, v[2:3]
	s_waitcnt vmcnt(11)
; __device__ __forceinline__ unsigned cvt_pk_bf16(float lo, float hi) { unsigned r; asm volatile("v_cvt_pk_bf16_f32 %0, %1, %2" : "=v"(r) : "v"(lo), "v"(hi)); return r; }
; __device__ __forceinline__ float bf_lo(unsigned w) { return __uint_as_float(w << 16); }
; __device__ __forceinline__ float bf_hi(unsigned w) { return __uint_as_float(w & 0xffff0000u); }
;     __device__ __forceinline__ void operator()(const f32x4 (&acc)[2][2][4][2], const Unit& u, int wr, int wc, int fr, int fq) const {
;         const int row0 = u.pm * BM + wr * 64 + fr; const int col0 = u.pn * BM + wc * 32 + 8 * fq;
; #pragma unroll
;         for (int ai = 0; ai < 2; ++ai)
; #pragma unroll
;             for (int m = 0; m < 4; ++m) { const size_t row = (size_t)(row0 + ai * HALF + m * 16);
; #pragma unroll
;                 for (int bj = 0; bj < 2; ++bj) { const int col = col0 + bj * HALF; const u32x4 g = *(const u32x4*)(G + row * ldg + col);
;                     const f32x4 a0 = acc[ai][bj][m][0] * P5_ACC_SCALE, a1 = acc[ai][bj][m][1] * P5_ACC_SCALE;
;                     const f32x4 o0 = {a0[0] * bf_lo(g.x), a0[1] * bf_hi(g.x), a0[2] * bf_lo(g.y), a0[3] * bf_hi(g.y)};
;                     const f32x4 o1 = {a1[0] * bf_lo(g.z), a1[1] * bf_hi(g.z), a1[2] * bf_lo(g.w), a1[3] * bf_hi(g.w)};
;                     u32x4 w; w.x = cvt_pk_bf16(o0[0], o0[1]); w.y = cvt_pk_bf16(o0[2], o0[3]); w.z = cvt_pk_bf16(o1[0], o1[1]); w.w = cvt_pk_bf16(o1[2], o1[3]);
;                     *(u32x4*)(M1 + row * 2048 + col) = w; } }
;     }
	v_lshlrev_b32_e32 v236, 16, v220
	v_and_b32_e32 v237, 0xffff0000, v220
	v_lshlrev_b32_e32 v238, 16, v221
	v_and_b32_e32 v239, 0xffff0000, v221
	v_lshlrev_b32_e32 v240, 16, v222
	v_and_b32_e32 v241, 0xffff0000, v222
	v_lshlrev_b32_e32 v242, 16, v223
	v_and_b32_e32 v243, 0xffff0000, v223
	v_pk_mul_f32 v[244:245], v[126:127], s[42:43] op_sel_hi:[1,0]
	v_pk_mul_f32 v[248:249], v[128:129], s[42:43] op_sel_hi:[1,0]
	v_pk_mul_f32 v[250:251], v[122:123], s[42:43] op_sel_hi:[1,0]
	v_pk_mul_f32 v[252:253], v[124:125], s[42:43] op_sel_hi:[1,0]
	v_pk_mul_f32 v[244:245], v[244:245], v[236:237]
	v_pk_mul_f32 v[248:249], v[248:249], v[238:239]
	v_pk_mul_f32 v[250:251], v[250:251], v[240:241]
	v_pk_mul_f32 v[252:253], v[252:253], v[242:243]
	v_cvt_pk_bf16_f32 v220, v244, v245
	v_cvt_pk_bf16_f32 v221, v248, v249
	v_cvt_pk_bf16_f32 v222, v250, v251
	v_cvt_pk_bf16_f32 v223, v252, v253
	global_store_dwordx4 v[30:31], v[220:223], off
	v_add_u32_e32 v32, 0xa0, v4
	v_mad_i64_i32 v[254:255], s[82:83], v32, s68, v[6:7]
	v_lshl_add_u64 v[254:255], v[254:255], 0, v[2:3]
	global_load_dwordx4 v[220:223], v[254:255], off
	s_waitcnt vmcnt(12)
	v_lshlrev_b32_e32 v236, 16, v224
	v_and_b32_e32 v237, 0xffff0000, v224
	v_lshlrev_b32_e32 v238, 16, v225
	v_and_b32_e32 v239, 0xffff0000, v225
	v_lshlrev_b32_e32 v240, 16, v226
	v_and_b32_e32 v241, 0xffff0000, v226
	v_lshlrev_b32_e32 v242, 16, v227
	v_and_b32_e32 v243, 0xffff0000, v227
	v_pk_mul_f32 v[244:245], v[118:119], s[42:43] op_sel_hi:[1,0]
	v_pk_mul_f32 v[248:249], v[120:121], s[42:43] op_sel_hi:[1,0]
	v_pk_mul_f32 v[250:251], v[114:115], s[42:43] op_sel_hi:[1,0]
	v_pk_mul_f32 v[252:253], v[116:117], s[42:43] op_sel_hi:[1,0]
	v_pk_mul_f32 v[244:245], v[244:245], v[236:237]
	v_pk_mul_f32 v[248:249], v[248:249], v[238:239]
	v_pk_mul_f32 v[250:251], v[250:251], v[240:241]
	v_pk_mul_f32 v[252:253], v[252:253], v[242:243]
	v_cvt_pk_bf16_f32 v224, v244, v245
	v_cvt_pk_bf16_f32 v225, v248, v249
	v_cvt_pk_bf16_f32 v226, v250, v251
	v_cvt_pk_bf16_f32 v227, v252, v253
	global_store_dwordx4 v[30:31], v[224:227], off offset:256
	global_load_dwordx4 v[224:227], v[254:255], off offset:256
	v_add_u32_e32 v33, 0x30, v4
	v_lshlrev_b32_e32 v30, 12, v33
	v_mov_b32_e32 v31, 0
	v_lshl_add_u64 v[30:31], s[8:9], 0, v[30:31]
	v_lshl_add_u64 v[30:31], v[30:31], 0, v[2:3]
	s_waitcnt vmcnt(13)
	v_lshlrev_b32_e32 v236, 16, v228
	v_and_b32_e32 v237, 0xffff0000, v228
	v_lshlrev_b32_e32 v238, 16, v229
	v_and_b32_e32 v239, 0xffff0000, v229
	v_lshlrev_b32_e32 v240, 16, v230
	v_and_b32_e32 v241, 0xffff0000, v230
	v_lshlrev_b32_e32 v242, 16, v231
	v_and_b32_e32 v243, 0xffff0000, v231
	v_pk_mul_f32 v[244:245], v[110:111], s[42:43] op_sel_hi:[1,0]
	v_pk_mul_f32 v[248:249], v[112:113], s[42:43] op_sel_hi:[1,0]
	v_pk_mul_f32 v[250:251], v[106:107], s[42:43] op_sel_hi:[1,0]
	v_pk_mul_f32 v[252:253], v[108:109], s[42:43] op_sel_hi:[1,0]
	v_pk_mul_f32 v[244:245], v[244:245], v[236:237]
	v_pk_mul_f32 v[248:249], v[248:249], v[238:239]
	v_pk_mul_f32 v[250:251], v[250:251], v[240:241]
	v_pk_mul_f32 v[252:253], v[252:253], v[242:243]
	v_cvt_pk_bf16_f32 v228, v244, v245
	v_cvt_pk_bf16_f32 v229, v248, v249
	v_cvt_pk_bf16_f32 v230, v250, v251
	v_cvt_pk_bf16_f32 v231, v252, v253
	global_store_dwordx4 v[30:31], v[228:231], off
	v_add_u32_e32 v32, 0xb0, v4
	v_mad_i64_i32 v[254:255], s[82:83], v32, s68, v[6:7]
	v_lshl_add_u64 v[254:255], v[254:255], 0, v[2:3]
	global_load_dwordx4 v[228:231], v[254:255], off
	s_waitcnt vmcnt(14)
	v_lshlrev_b32_e32 v236, 16, v232
	v_and_b32_e32 v237, 0xffff0000, v232
	v_lshlrev_b32_e32 v238, 16, v233
	v_and_b32_e32 v239, 0xffff0000, v233
	v_lshlrev_b32_e32 v240, 16, v234
	v_and_b32_e32 v241, 0xffff0000, v234
	v_lshlrev_b32_e32 v242, 16, v235
	v_and_b32_e32 v243, 0xffff0000, v235
	v_pk_mul_f32 v[244:245], v[102:103], s[42:43] op_sel_hi:[1,0]
	v_pk_mul_f32 v[248:249], v[104:105], s[42:43] op_sel_hi:[1,0]
	v_pk_mul_f32 v[250:251], v[98:99], s[42:43] op_sel_hi:[1,0]
	v_pk_mul_f32 v[252:253], v[100:101], s[42:43] op_sel_hi:[1,0]
	v_pk_mul_f32 v[244:245], v[244:245], v[236:237]
	v_pk_mul_f32 v[248:249], v[248:249], v[238:239]
	v_pk_mul_f32 v[250:251], v[250:251], v[240:241]
	v_pk_mul_f32 v[252:253], v[252:253], v[242:243]
	v_cvt_pk_bf16_f32 v232, v244, v245
	v_cvt_pk_bf16_f32 v233, v248, v249
	v_cvt_pk_bf16_f32 v234, v250, v251
	v_cvt_pk_bf16_f32 v235, v252, v253
	global_store_dwordx4 v[30:31], v[232:235], off offset:256
	global_load_dwordx4 v[232:235], v[254:255], off offset:256
	v_add_u32_e32 v33, 0x80, v4
	v_lshlrev_b32_e32 v30, 12, v33
	v_mov_b32_e32 v31, 0
	v_lshl_add_u64 v[30:31], s[8:9], 0, v[30:31]
	v_lshl_add_u64 v[30:31], v[30:31], 0, v[2:3]
	s_waitcnt vmcnt(14)
	v_lshlrev_b32_e32 v236, 16, v204
	v_and_b32_e32 v237, 0xffff0000, v204
	v_lshlrev_b32_e32 v238, 16, v205
	v_and_b32_e32 v239, 0xffff0000, v205
	v_lshlrev_b32_e32 v240, 16, v206
	v_and_b32_e32 v241, 0xffff0000, v206
	v_lshlrev_b32_e32 v242, 16, v207
	v_and_b32_e32 v243, 0xffff0000, v207
	v_pk_mul_f32 v[244:245], v[94:95], s[42:43] op_sel_hi:[1,0]
	v_pk_mul_f32 v[248:249], v[96:97], s[42:43] op_sel_hi:[1,0]
	v_pk_mul_f32 v[250:251], v[90:91], s[42:43] op_sel_hi:[1,0]
	v_pk_mul_f32 v[252:253], v[92:93], s[42:43] op_sel_hi:[1,0]
	v_pk_mul_f32 v[244:245], v[244:245], v[236:237]
	v_pk_mul_f32 v[248:249], v[248:249], v[238:239]
	v_pk_mul_f32 v[250:251], v[250:251], v[240:241]
	v_pk_mul_f32 v[252:253], v[252:253], v[242:243]
	v_cvt_pk_bf16_f32 v204, v244, v245
	v_cvt_pk_bf16_f32 v205, v248, v249
	v_cvt_pk_bf16_f32 v206, v250, v251
	v_cvt_pk_bf16_f32 v207, v252, v253
	global_store_dwordx4 v[30:31], v[204:207], off
	s_waitcnt vmcnt(13)
; __device__ __forceinline__ unsigned cvt_pk_bf16(float lo, float hi) { unsigned r; asm volatile("v_cvt_pk_bf16_f32 %0, %1, %2" : "=v"(r) : "v"(lo), "v"(hi)); return r; }
; __device__ __forceinline__ float bf_lo(unsigned w) { return __uint_as_float(w << 16); }
; __device__ __forceinline__ float bf_hi(unsigned w) { return __uint_as_float(w & 0xffff0000u); }
;     __device__ __forceinline__ void operator()(const f32x4 (&acc)[2][2][4][2], const Unit& u, int wr, int wc, int fr, int fq) const {
;         const int row0 = u.pm * BM + wr * 64 + fr; const int col0 = u.pn * BM + wc * 32 + 8 * fq;
; #pragma unroll
;         for (int ai = 0; ai < 2; ++ai)
; #pragma unroll
;             for (int m = 0; m < 4; ++m) { const size_t row = (size_t)(row0 + ai * HALF + m * 16);
; #pragma unroll
;                 for (int bj = 0; bj < 2; ++bj) { const int col = col0 + bj * HALF; const u32x4 g = *(const u32x4*)(G + row * ldg + col);
;                     const f32x4 a0 = acc[ai][bj][m][0] * P5_ACC_SCALE, a1 = acc[ai][bj][m][1] * P5_ACC_SCALE;
;                     const f32x4 o0 = {a0[0] * bf_lo(g.x), a0[1] * bf_hi(g.x), a0[2] * bf_lo(g.y), a0[3] * bf_hi(g.y)};
;                     const f32x4 o1 = {a1[0] * bf_lo(g.z), a1[1] * bf_hi(g.z), a1[2] * bf_lo(g.w), a1[3] * bf_hi(g.w)};
;                     u32x4 w; w.x = cvt_pk_bf16(o0[0], o0[1]); w.y = cvt_pk_bf16(o0[2], o0[3]); w.z = cvt_pk_bf16(o1[0], o1[1]); w.w = cvt_pk_bf16(o1[2], o1[3]);
;                     *(u32x4*)(M1 + row * 2048 + col) = w; } }
;     }
	v_lshlrev_b32_e32 v236, 16, v208
	v_and_b32_e32 v237, 0xffff0000, v208
	v_lshlrev_b32_e32 v238, 16, v209
	v_and_b32_e32 v239, 0xffff0000, v209
	v_lshlrev_b32_e32 v240, 16, v210
	v_and_b32_e32 v241, 0xffff0000, v210
	v_lshlrev_b32_e32 v242, 16, v211
	v_and_b32_e32 v243, 0xffff0000, v211
	v_pk_mul_f32 v[244:245], v[86:87], s[42:43] op_sel_hi:[1,0]
	v_pk_mul_f32 v[248:249], v[88:89], s[42:43] op_sel_hi:[1,0]
	v_pk_mul_f32 v[250:251], v[82:83], s[42:43] op_sel_hi:[1,0]
	v_pk_mul_f32 v[252:253], v[84:85], s[42:43] op_sel_hi:[1,0]
	v_pk_mul_f32 v[244:245], v[244:245], v[236:237]
	v_pk_mul_f32 v[248:249], v[248:249], v[238:239]
	v_pk_mul_f32 v[250:251], v[250:251], v[240:241]
	v_pk_mul_f32 v[252:253], v[252:253], v[242:243]
	v_cvt_pk_bf16_f32 v208, v244, v245
	v_cvt_pk_bf16_f32 v209, v248, v249
	v_cvt_pk_bf16_f32 v210, v250, v251
	v_cvt_pk_bf16_f32 v211, v252, v253
	global_store_dwordx4 v[30:31], v[208:211], off offset:256
	v_add_u32_e32 v33, 0x90, v4
	v_lshlrev_b32_e32 v30, 12, v33
	v_mov_b32_e32 v31, 0
	v_lshl_add_u64 v[30:31], s[8:9], 0, v[30:31]
	v_lshl_add_u64 v[30:31], v[30:31], 0, v[2:3]
	s_waitcnt vmcnt(12)
	v_lshlrev_b32_e32 v236, 16, v212
	v_and_b32_e32 v237, 0xffff0000, v212
	v_lshlrev_b32_e32 v238, 16, v213
	v_and_b32_e32 v239, 0xffff0000, v213
	v_lshlrev_b32_e32 v240, 16, v214
	v_and_b32_e32 v241, 0xffff0000, v214
	v_lshlrev_b32_e32 v242, 16, v215
	v_and_b32_e32 v243, 0xffff0000, v215
	v_pk_mul_f32 v[244:245], v[78:79], s[42:43] op_sel_hi:[1,0]
	v_pk_mul_f32 v[248:249], v[80:81], s[42:43] op_sel_hi:[1,0]
	v_pk_mul_f32 v[250:251], v[74:75], s[42:43] op_sel_hi:[1,0]
	v_pk_mul_f32 v[252:253], v[76:77], s[42:43] op_sel_hi:[1,0]
	v_pk_mul_f32 v[244:245], v[244:245], v[236:237]
	v_pk_mul_f32 v[248:249], v[248:249], v[238:239]
	v_pk_mul_f32 v[250:251], v[250:251], v[240:241]
	v_pk_mul_f32 v[252:253], v[252:253], v[242:243]
	v_cvt_pk_bf16_f32 v212, v244, v245
	v_cvt_pk_bf16_f32 v213, v248, v249
	v_cvt_pk_bf16_f32 v214, v250, v251
	v_cvt_pk_bf16_f32 v215, v252, v253
	global_store_dwordx4 v[30:31], v[212:215], off
	s_waitcnt vmcnt(11)
	v_lshlrev_b32_e32 v236, 16, v216
	v_and_b32_e32 v237, 0xffff0000, v216
	v_lshlrev_b32_e32 v238, 16, v217
	v_and_b32_e32 v239, 0xffff0000, v217
	v_lshlrev_b32_e32 v240, 16, v218
	v_and_b32_e32 v241, 0xffff0000, v218
	v_lshlrev_b32_e32 v242, 16, v219
	v_and_b32_e32 v243, 0xffff0000, v219
	v_pk_mul_f32 v[244:245], v[70:71], s[42:43] op_sel_hi:[1,0]
	v_pk_mul_f32 v[248:249], v[72:73], s[42:43] op_sel_hi:[1,0]
	v_pk_mul_f32 v[250:251], v[66:67], s[42:43] op_sel_hi:[1,0]
	v_pk_mul_f32 v[252:253], v[68:69], s[42:43] op_sel_hi:[1,0]
	v_pk_mul_f32 v[244:245], v[244:245], v[236:237]
	v_pk_mul_f32 v[248:249], v[248:249], v[238:239]
	v_pk_mul_f32 v[250:251], v[250:251], v[240:241]
	v_pk_mul_f32 v[252:253], v[252:253], v[242:243]
	v_cvt_pk_bf16_f32 v216, v244, v245
	v_cvt_pk_bf16_f32 v217, v248, v249
	v_cvt_pk_bf16_f32 v218, v250, v251
	v_cvt_pk_bf16_f32 v219, v252, v253
	global_store_dwordx4 v[30:31], v[216:219], off offset:256
	v_add_u32_e32 v33, 0xa0, v4
	v_lshlrev_b32_e32 v30, 12, v33
	v_mov_b32_e32 v31, 0
	v_lshl_add_u64 v[30:31], s[8:9], 0, v[30:31]
	v_lshl_add_u64 v[30:31], v[30:31], 0, v[2:3]
	s_waitcnt vmcnt(10)
; __device__ __forceinline__ unsigned cvt_pk_bf16(float lo, float hi) { unsigned r; asm volatile("v_cvt_pk_bf16_f32 %0, %1, %2" : "=v"(r) : "v"(lo), "v"(hi)); return r; }
; __device__ __forceinline__ float bf_lo(unsigned w) { return __uint_as_float(w << 16); }
; __device__ __forceinline__ float bf_hi(unsigned w) { return __uint_as_float(w & 0xffff0000u); }
;     __device__ __forceinline__ void operator()(const f32x4 (&acc)[2][2][4][2], const Unit& u, int wr, int wc, int fr, int fq) const {
;         const int row0 = u.pm * BM + wr * 64 + fr; const int col0 = u.pn * BM + wc * 32 + 8 * fq;
; #pragma unroll
;         for (int ai = 0; ai < 2; ++ai)
; #pragma unroll
;             for (int m = 0; m < 4; ++m) { const size_t row = (size_t)(row0 + ai * HALF + m * 16);
; #pragma unroll
;                 for (int bj = 0; bj < 2; ++bj) { const int col = col0 + bj * HALF; const u32x4 g = *(const u32x4*)(G + row * ldg + col);
;                     const f32x4 a0 = acc[ai][bj][m][0] * P5_ACC_SCALE, a1 = acc[ai][bj][m][1] * P5_ACC_SCALE;
;                     const f32x4 o0 = {a0[0] * bf_lo(g.x), a0[1] * bf_hi(g.x), a0[2] * bf_lo(g.y), a0[3] * bf_hi(g.y)};
;                     const f32x4 o1 = {a1[0] * bf_lo(g.z), a1[1] * bf_hi(g.z), a1[2] * bf_lo(g.w), a1[3] * bf_hi(g.w)};
;                     u32x4 w; w.x = cvt_pk_bf16(o0[0], o0[1]); w.y = cvt_pk_bf16(o0[2], o0[3]); w.z = cvt_pk_bf16(o1[0], o1[1]); w.w = cvt_pk_bf16(o1[2], o1[3]);
;                     *(u32x4*)(M1 + row * 2048 + col) = w; } }
;     }
	v_lshlrev_b32_e32 v236, 16, v220
	v_and_b32_e32 v237, 0xffff0000, v220
	v_lshlrev_b32_e32 v238, 16, v221
	v_and_b32_e32 v239, 0xffff0000, v221
	v_lshlrev_b32_e32 v240, 16, v222
	v_and_b32_e32 v241, 0xffff0000, v222
	v_lshlrev_b32_e32 v242, 16, v223
	v_and_b32_e32 v243, 0xffff0000, v223
	v_pk_mul_f32 v[244:245], v[62:63], s[42:43] op_sel_hi:[1,0]
	v_pk_mul_f32 v[248:249], v[64:65], s[42:43] op_sel_hi:[1,0]
	v_pk_mul_f32 v[250:251], v[58:59], s[42:43] op_sel_hi:[1,0]
	v_pk_mul_f32 v[252:253], v[60:61], s[42:43] op_sel_hi:[1,0]
	v_pk_mul_f32 v[244:245], v[244:245], v[236:237]
	v_pk_mul_f32 v[248:249], v[248:249], v[238:239]
	v_pk_mul_f32 v[250:251], v[250:251], v[240:241]
	v_pk_mul_f32 v[252:253], v[252:253], v[242:243]
	v_cvt_pk_bf16_f32 v220, v244, v245
	v_cvt_pk_bf16_f32 v221, v248, v249
	v_cvt_pk_bf16_f32 v222, v250, v251
	v_cvt_pk_bf16_f32 v223, v252, v253
	global_store_dwordx4 v[30:31], v[220:223], off
	s_waitcnt vmcnt(9)
	v_lshlrev_b32_e32 v236, 16, v224
	v_and_b32_e32 v237, 0xffff0000, v224
	v_lshlrev_b32_e32 v238, 16, v225
	v_and_b32_e32 v239, 0xffff0000, v225
	v_lshlrev_b32_e32 v240, 16, v226
	v_and_b32_e32 v241, 0xffff0000, v226
	v_lshlrev_b32_e32 v242, 16, v227
	v_and_b32_e32 v243, 0xffff0000, v227
	v_pk_mul_f32 v[244:245], v[54:55], s[42:43] op_sel_hi:[1,0]
	v_pk_mul_f32 v[248:249], v[56:57], s[42:43] op_sel_hi:[1,0]
	v_pk_mul_f32 v[250:251], v[50:51], s[42:43] op_sel_hi:[1,0]
	v_pk_mul_f32 v[252:253], v[52:53], s[42:43] op_sel_hi:[1,0]
	v_pk_mul_f32 v[244:245], v[244:245], v[236:237]
	v_pk_mul_f32 v[248:249], v[248:249], v[238:239]
	v_pk_mul_f32 v[250:251], v[250:251], v[240:241]
	v_pk_mul_f32 v[252:253], v[252:253], v[242:243]
	v_cvt_pk_bf16_f32 v224, v244, v245
	v_cvt_pk_bf16_f32 v225, v248, v249
	v_cvt_pk_bf16_f32 v226, v250, v251
	v_cvt_pk_bf16_f32 v227, v252, v253
	global_store_dwordx4 v[30:31], v[224:227], off offset:256
	v_add_u32_e32 v33, 0xb0, v4
	v_lshlrev_b32_e32 v30, 12, v33
	v_mov_b32_e32 v31, 0
	v_lshl_add_u64 v[30:31], s[8:9], 0, v[30:31]
	v_lshl_add_u64 v[30:31], v[30:31], 0, v[2:3]
	s_waitcnt vmcnt(8)
	v_lshlrev_b32_e32 v236, 16, v228
	v_and_b32_e32 v237, 0xffff0000, v228
	v_lshlrev_b32_e32 v238, 16, v229
	v_and_b32_e32 v239, 0xffff0000, v229
	v_lshlrev_b32_e32 v240, 16, v230
	v_and_b32_e32 v241, 0xffff0000, v230
	v_lshlrev_b32_e32 v242, 16, v231
	v_and_b32_e32 v243, 0xffff0000, v231
	v_pk_mul_f32 v[244:245], v[46:47], s[42:43] op_sel_hi:[1,0]
	v_pk_mul_f32 v[248:249], v[48:49], s[42:43] op_sel_hi:[1,0]
	v_pk_mul_f32 v[250:251], v[42:43], s[42:43] op_sel_hi:[1,0]
	v_pk_mul_f32 v[252:253], v[44:45], s[42:43] op_sel_hi:[1,0]
	v_pk_mul_f32 v[244:245], v[244:245], v[236:237]
	v_pk_mul_f32 v[248:249], v[248:249], v[238:239]
	v_pk_mul_f32 v[250:251], v[250:251], v[240:241]
	v_pk_mul_f32 v[252:253], v[252:253], v[242:243]
	v_cvt_pk_bf16_f32 v228, v244, v245
	v_cvt_pk_bf16_f32 v229, v248, v249
	v_cvt_pk_bf16_f32 v230, v250, v251
	v_cvt_pk_bf16_f32 v231, v252, v253
	global_store_dwordx4 v[30:31], v[228:231], off
	s_waitcnt vmcnt(7)
	v_lshlrev_b32_e32 v236, 16, v232
	v_and_b32_e32 v237, 0xffff0000, v232
	v_lshlrev_b32_e32 v238, 16, v233
	v_and_b32_e32 v239, 0xffff0000, v233
	v_lshlrev_b32_e32 v240, 16, v234
	v_and_b32_e32 v241, 0xffff0000, v234
	v_lshlrev_b32_e32 v242, 16, v235
	v_and_b32_e32 v243, 0xffff0000, v235
	v_pk_mul_f32 v[244:245], v[38:39], s[42:43] op_sel_hi:[1,0]
	v_pk_mul_f32 v[248:249], v[40:41], s[42:43] op_sel_hi:[1,0]
	v_pk_mul_f32 v[250:251], v[34:35], s[42:43] op_sel_hi:[1,0]
	v_pk_mul_f32 v[252:253], v[36:37], s[42:43] op_sel_hi:[1,0]
	v_pk_mul_f32 v[244:245], v[244:245], v[236:237]
	v_pk_mul_f32 v[248:249], v[248:249], v[238:239]
	v_pk_mul_f32 v[250:251], v[250:251], v[240:241]
	v_pk_mul_f32 v[252:253], v[252:253], v[242:243]
	v_cvt_pk_bf16_f32 v232, v244, v245
	v_cvt_pk_bf16_f32 v233, v248, v249
	v_cvt_pk_bf16_f32 v234, v250, v251
	v_cvt_pk_bf16_f32 v235, v252, v253
	global_store_dwordx4 v[30:31], v[232:235], off offset:256
	s_cbranch_vccnz .LBB0_722
	s_andn2_b64 vcc, exec, s[22:23]
	s_cbranch_vccnz .LBB0_721
	s_barrier
	s_branch .LBB0_721

; __device__ __forceinline__ float bf_lo(unsigned w) { return __uint_as_float(w << 16); }
; __device__ __forceinline__ float bf_hi(unsigned w) { return __uint_as_float(w & 0xffff0000u); }
;     __device__ __forceinline__ void operator()(const f32x4 (&acc)[2][2][4][2], const Unit& u, int wr, int wc, int fr, int fq) const {
;         const int row0 = u.pm * BM + wr * 64 + fr; const int col0 = u.pn * BM + wc * 32 + 8 * fq;
; #pragma unroll
;         for (int ai = 0; ai < 2; ++ai)
; #pragma unroll
;             for (int m = 0; m < 4; ++m) { const size_t row = (size_t)(row0 + ai * HALF + m * 16);
; #pragma unroll
;                 for (int bj = 0; bj < 2; ++bj) { const int col = col0 + bj * HALF; const u32x4 g = *(const u32x4*)(G + row * ldg + col);
;                     const u32x4 mw = *(const u32x4*)(M1 + row * 2048 + col);
;                     const f32x4 m0 = {bf_lo(mw.x), bf_hi(mw.x), bf_lo(mw.y), bf_hi(mw.y)}, m1 = {bf_lo(mw.z), bf_hi(mw.z), bf_lo(mw.w), bf_hi(mw.w)};
;                     const f32x4 a0 = acc[ai][bj][m][0] * P5_ACC_SCALE, a1 = acc[ai][bj][m][1] * P5_ACC_SCALE;
;                     const f32x4 o0 = {m0[0] + a0[0] * bf_lo(g.x), m0[1] + a0[1] * bf_hi(g.x), m0[2] + a0[2] * bf_lo(g.y), m0[3] + a0[3] * bf_hi(g.y)};
;                     const f32x4 o1 = {m1[0] + a1[0] * bf_lo(g.z), m1[1] + a1[1] * bf_hi(g.z), m1[2] + a1[2] * bf_lo(g.w), m1[3] + a1[3] * bf_hi(g.w)};
;                     int w0 = __builtin_amdgcn_cvt_pk_fp8_f32(o0[0] * 16.f, o0[1] * 16.f, 0, false); w0 = __builtin_amdgcn_cvt_pk_fp8_f32(o0[2] * 16.f, o0[3] * 16.f, w0, true);
;                     int w1 = __builtin_amdgcn_cvt_pk_fp8_f32(o1[0] * 16.f, o1[1] * 16.f, 0, false); w1 = __builtin_amdgcn_cvt_pk_fp8_f32(o1[2] * 16.f, o1[3] * 16.f, w1, true);
;                     typedef int v2i_m __attribute__((ext_vector_type(2))); *(v2i_m*)(MG + row * 2048 + col) = (v2i_m){w0, w1}; } }
;     }
.LBB0_753:
	v_lshl_add_u32 v8, s56, 8, v191
	v_lshl_or_b32 v2, s64, 8, v193
	v_ashrrev_i32_e32 v9, 31, v8
	v_mov_b64_e32 v[4:5], s[18:19]
	v_ashrrev_i32_e32 v3, 31, v2
	v_lshlrev_b64 v[14:15], 12, v[8:9]
	v_mad_i64_i32 v[10:11], s[58:59], v8, s57, v[4:5]
	v_lshlrev_b64 v[6:7], 1, v[2:3]
	v_lshl_add_u64 v[14:15], s[8:9], 0, v[14:15]
	v_lshl_add_u64 v[18:19], v[10:11], 0, v[6:7]
	v_lshl_add_u64 v[20:21], v[14:15], 0, v[6:7]
	s_andn2_b64 vcc, exec, s[4:5]
	s_mov_b64 s[4:5], -1
	s_mov_b32 s84, 0x41800000
	s_mov_b32 s85, 0x41800000
	v_add_u32_e32 v242, 0x0, v8
	v_mad_i64_i32 v[236:237], s[82:83], v242, s57, v[4:5]
	v_lshl_add_u64 v[236:237], v[236:237], 0, v[6:7]
	v_lshlrev_b32_e32 v238, 12, v242
	v_mov_b32_e32 v239, 0
	v_lshl_add_u64 v[238:239], s[8:9], 0, v[238:239]
	v_lshl_add_u64 v[238:239], v[238:239], 0, v[6:7]
	global_load_dwordx4 v[204:207], v[236:237], off
	global_load_dwordx4 v[220:223], v[238:239], off
	global_load_dwordx4 v[208:211], v[236:237], off offset:256
	global_load_dwordx4 v[224:227], v[238:239], off offset:256
	v_add_u32_e32 v242, 0x10, v8
	v_mad_i64_i32 v[236:237], s[82:83], v242, s57, v[4:5]
	v_lshl_add_u64 v[236:237], v[236:237], 0, v[6:7]
	v_lshlrev_b32_e32 v238, 12, v242
	v_mov_b32_e32 v239, 0
	v_lshl_add_u64 v[238:239], s[8:9], 0, v[238:239]
	v_lshl_add_u64 v[238:239], v[238:239], 0, v[6:7]
	global_load_dwordx4 v[212:215], v[236:237], off
	global_load_dwordx4 v[228:231], v[238:239], off
	global_load_dwordx4 v[216:219], v[236:237], off offset:256
	global_load_dwordx4 v[232:235], v[238:239], off offset:256
	v_add_u32_e32 v243, 0x0, v8
	v_lshlrev_b32_e32 v240, 11, v243
	v_mov_b32_e32 v241, 0
	v_lshl_add_u64 v[240:241], s[22:23], 0, v[240:241]
	v_lshl_add_u64 v[240:241], v[240:241], 0, v[2:3]
	s_waitcnt vmcnt(6)
	v_lshlrev_b32_e32 v10, 16, v204
	v_and_b32_e32 v11, 0xffff0000, v204
	v_lshlrev_b32_e32 v18, 16, v220
	v_and_b32_e32 v19, 0xffff0000, v220
	v_lshlrev_b32_e32 v12, 16, v205
	v_and_b32_e32 v13, 0xffff0000, v205
	v_lshlrev_b32_e32 v20, 16, v221
	v_and_b32_e32 v21, 0xffff0000, v221
	v_lshlrev_b32_e32 v14, 16, v206
	v_and_b32_e32 v15, 0xffff0000, v206
	v_lshlrev_b32_e32 v22, 16, v222
	v_and_b32_e32 v23, 0xffff0000, v222
	v_lshlrev_b32_e32 v16, 16, v207
	v_and_b32_e32 v17, 0xffff0000, v207
	v_lshlrev_b32_e32 v24, 16, v223
	v_and_b32_e32 v25, 0xffff0000, v223
	v_pk_mul_f32 v[26:27], v[158:159], s[40:41] op_sel_hi:[1,0]
	v_pk_mul_f32 v[28:29], v[160:161], s[40:41] op_sel_hi:[1,0]
	v_pk_mul_f32 v[30:31], v[154:155], s[40:41] op_sel_hi:[1,0]
	v_pk_mul_f32 v[32:33], v[156:157], s[40:41] op_sel_hi:[1,0]
	v_pk_fma_f32 v[26:27], v[26:27], v[10:11], v[18:19]
	v_pk_fma_f32 v[28:29], v[28:29], v[12:13], v[20:21]
	v_pk_fma_f32 v[30:31], v[30:31], v[14:15], v[22:23]
	v_pk_fma_f32 v[32:33], v[32:33], v[16:17], v[24:25]
	v_pk_mul_f32 v[26:27], v[26:27], s[84:85] op_sel_hi:[1,0]
	v_pk_mul_f32 v[28:29], v[28:29], s[84:85] op_sel_hi:[1,0]
	v_pk_mul_f32 v[30:31], v[30:31], s[84:85] op_sel_hi:[1,0]
	v_pk_mul_f32 v[32:33], v[32:33], s[84:85] op_sel_hi:[1,0]
	s_nop 0
	v_cvt_pk_fp8_f32 v244, v26, v27
	v_cvt_pk_fp8_f32 v245, v30, v31
	s_nop 0
	v_cvt_pk_fp8_f32 v244, v28, v29 op_sel:[0,0,1]
	v_cvt_pk_fp8_f32 v245, v32, v33 op_sel:[0,0,1]
	global_store_dwordx2 v[240:241], v[244:245], off
	v_add_u32_e32 v242, 0x20, v8
	v_mad_i64_i32 v[236:237], s[82:83], v242, s57, v[4:5]
	v_lshl_add_u64 v[236:237], v[236:237], 0, v[6:7]
	v_lshlrev_b32_e32 v238, 12, v242
	v_mov_b32_e32 v239, 0
	v_lshl_add_u64 v[238:239], s[8:9], 0, v[238:239]
	v_lshl_add_u64 v[238:239], v[238:239], 0, v[6:7]
	global_load_dwordx4 v[204:207], v[236:237], off
	global_load_dwordx4 v[220:223], v[238:239], off
	s_waitcnt vmcnt(7)
	v_lshlrev_b32_e32 v10, 16, v208
	v_and_b32_e32 v11, 0xffff0000, v208
	v_lshlrev_b32_e32 v18, 16, v224
	v_and_b32_e32 v19, 0xffff0000, v224
	v_lshlrev_b32_e32 v12, 16, v209
	v_and_b32_e32 v13, 0xffff0000, v209
	v_lshlrev_b32_e32 v20, 16, v225
	v_and_b32_e32 v21, 0xffff0000, v225
	v_lshlrev_b32_e32 v14, 16, v210
	v_and_b32_e32 v15, 0xffff0000, v210
	v_lshlrev_b32_e32 v22, 16, v226
	v_and_b32_e32 v23, 0xffff0000, v226
	v_lshlrev_b32_e32 v16, 16, v211
	v_and_b32_e32 v17, 0xffff0000, v211
	v_lshlrev_b32_e32 v24, 16, v227
	v_and_b32_e32 v25, 0xffff0000, v227
	v_pk_mul_f32 v[26:27], v[150:151], s[40:41] op_sel_hi:[1,0]
	v_pk_mul_f32 v[28:29], v[152:153], s[40:41] op_sel_hi:[1,0]
	v_pk_mul_f32 v[30:31], v[146:147], s[40:41] op_sel_hi:[1,0]
	v_pk_mul_f32 v[32:33], v[148:149], s[40:41] op_sel_hi:[1,0]
	v_pk_fma_f32 v[26:27], v[26:27], v[10:11], v[18:19]
	v_pk_fma_f32 v[28:29], v[28:29], v[12:13], v[20:21]
	v_pk_fma_f32 v[30:31], v[30:31], v[14:15], v[22:23]
	v_pk_fma_f32 v[32:33], v[32:33], v[16:17], v[24:25]
	v_pk_mul_f32 v[26:27], v[26:27], s[84:85] op_sel_hi:[1,0]
	v_pk_mul_f32 v[28:29], v[28:29], s[84:85] op_sel_hi:[1,0]
	v_pk_mul_f32 v[30:31], v[30:31], s[84:85] op_sel_hi:[1,0]
	v_pk_mul_f32 v[32:33], v[32:33], s[84:85] op_sel_hi:[1,0]
	s_nop 0
	v_cvt_pk_fp8_f32 v248, v26, v27
	v_cvt_pk_fp8_f32 v249, v30, v31
	s_nop 0
	v_cvt_pk_fp8_f32 v248, v28, v29 op_sel:[0,0,1]
	v_cvt_pk_fp8_f32 v249, v32, v33 op_sel:[0,0,1]
	global_store_dwordx2 v[240:241], v[248:249], off offset:128
	global_load_dwordx4 v[208:211], v[236:237], off offset:256
	global_load_dwordx4 v[224:227], v[238:239], off offset:256
	v_add_u32_e32 v243, 0x10, v8
	v_lshlrev_b32_e32 v240, 11, v243
	v_mov_b32_e32 v241, 0
	v_lshl_add_u64 v[240:241], s[22:23], 0, v[240:241]
	v_lshl_add_u64 v[240:241], v[240:241], 0, v[2:3]
	s_waitcnt vmcnt(8)
; __device__ __forceinline__ float bf_lo(unsigned w) { return __uint_as_float(w << 16); }
; __device__ __forceinline__ float bf_hi(unsigned w) { return __uint_as_float(w & 0xffff0000u); }
;     __device__ __forceinline__ void operator()(const f32x4 (&acc)[2][2][4][2], const Unit& u, int wr, int wc, int fr, int fq) const {
;         const int row0 = u.pm * BM + wr * 64 + fr; const int col0 = u.pn * BM + wc * 32 + 8 * fq;
; #pragma unroll
;         for (int ai = 0; ai < 2; ++ai)
; #pragma unroll
;             for (int m = 0; m < 4; ++m) { const size_t row = (size_t)(row0 + ai * HALF + m * 16);
; #pragma unroll
;                 for (int bj = 0; bj < 2; ++bj) { const int col = col0 + bj * HALF; const u32x4 g = *(const u32x4*)(G + row * ldg + col);
;                     const u32x4 mw = *(const u32x4*)(M1 + row * 2048 + col);
;                     const f32x4 m0 = {bf_lo(mw.x), bf_hi(mw.x), bf_lo(mw.y), bf_hi(mw.y)}, m1 = {bf_lo(mw.z), bf_hi(mw.z), bf_lo(mw.w), bf_hi(mw.w)};
;                     const f32x4 a0 = acc[ai][bj][m][0] * P5_ACC_SCALE, a1 = acc[ai][bj][m][1] * P5_ACC_SCALE;
;                     const f32x4 o0 = {m0[0] + a0[0] * bf_lo(g.x), m0[1] + a0[1] * bf_hi(g.x), m0[2] + a0[2] * bf_lo(g.y), m0[3] + a0[3] * bf_hi(g.y)};
;                     const f32x4 o1 = {m1[0] + a1[0] * bf_lo(g.z), m1[1] + a1[1] * bf_hi(g.z), m1[2] + a1[2] * bf_lo(g.w), m1[3] + a1[3] * bf_hi(g.w)};
;                     int w0 = __builtin_amdgcn_cvt_pk_fp8_f32(o0[0] * 16.f, o0[1] * 16.f, 0, false); w0 = __builtin_amdgcn_cvt_pk_fp8_f32(o0[2] * 16.f, o0[3] * 16.f, w0, true);
;                     int w1 = __builtin_amdgcn_cvt_pk_fp8_f32(o1[0] * 16.f, o1[1] * 16.f, 0, false); w1 = __builtin_amdgcn_cvt_pk_fp8_f32(o1[2] * 16.f, o1[3] * 16.f, w1, true);
;                     typedef int v2i_m __attribute__((ext_vector_type(2))); *(v2i_m*)(MG + row * 2048 + col) = (v2i_m){w0, w1}; } }
;     }
	v_lshlrev_b32_e32 v10, 16, v212
	v_and_b32_e32 v11, 0xffff0000, v212
	v_lshlrev_b32_e32 v18, 16, v228
	v_and_b32_e32 v19, 0xffff0000, v228
	v_lshlrev_b32_e32 v12, 16, v213
	v_and_b32_e32 v13, 0xffff0000, v213
	v_lshlrev_b32_e32 v20, 16, v229
	v_and_b32_e32 v21, 0xffff0000, v229
	v_lshlrev_b32_e32 v14, 16, v214
	v_and_b32_e32 v15, 0xffff0000, v214
	v_lshlrev_b32_e32 v22, 16, v230
	v_and_b32_e32 v23, 0xffff0000, v230
	v_lshlrev_b32_e32 v16, 16, v215
	v_and_b32_e32 v17, 0xffff0000, v215
	v_lshlrev_b32_e32 v24, 16, v231
	v_and_b32_e32 v25, 0xffff0000, v231
	v_pk_mul_f32 v[26:27], v[142:143], s[40:41] op_sel_hi:[1,0]
	v_pk_mul_f32 v[28:29], v[144:145], s[40:41] op_sel_hi:[1,0]
	v_pk_mul_f32 v[30:31], v[138:139], s[40:41] op_sel_hi:[1,0]
	v_pk_mul_f32 v[32:33], v[140:141], s[40:41] op_sel_hi:[1,0]
	v_pk_fma_f32 v[26:27], v[26:27], v[10:11], v[18:19]
	v_pk_fma_f32 v[28:29], v[28:29], v[12:13], v[20:21]
	v_pk_fma_f32 v[30:31], v[30:31], v[14:15], v[22:23]
	v_pk_fma_f32 v[32:33], v[32:33], v[16:17], v[24:25]
	v_pk_mul_f32 v[26:27], v[26:27], s[84:85] op_sel_hi:[1,0]
	v_pk_mul_f32 v[28:29], v[28:29], s[84:85] op_sel_hi:[1,0]
	v_pk_mul_f32 v[30:31], v[30:31], s[84:85] op_sel_hi:[1,0]
	v_pk_mul_f32 v[32:33], v[32:33], s[84:85] op_sel_hi:[1,0]
	s_nop 0
	v_cvt_pk_fp8_f32 v244, v26, v27
	v_cvt_pk_fp8_f32 v245, v30, v31
	s_nop 0
	v_cvt_pk_fp8_f32 v244, v28, v29 op_sel:[0,0,1]
	v_cvt_pk_fp8_f32 v245, v32, v33 op_sel:[0,0,1]
	global_store_dwordx2 v[240:241], v[244:245], off
	v_add_u32_e32 v242, 0x30, v8
	v_mad_i64_i32 v[236:237], s[82:83], v242, s57, v[4:5]
	v_lshl_add_u64 v[236:237], v[236:237], 0, v[6:7]
	v_lshlrev_b32_e32 v238, 12, v242
	v_mov_b32_e32 v239, 0
	v_lshl_add_u64 v[238:239], s[8:9], 0, v[238:239]
	v_lshl_add_u64 v[238:239], v[238:239], 0, v[6:7]
	global_load_dwordx4 v[212:215], v[236:237], off
	global_load_dwordx4 v[228:231], v[238:239], off
	s_waitcnt vmcnt(9)
	v_lshlrev_b32_e32 v10, 16, v216
	v_and_b32_e32 v11, 0xffff0000, v216
	v_lshlrev_b32_e32 v18, 16, v232
	v_and_b32_e32 v19, 0xffff0000, v232
	v_lshlrev_b32_e32 v12, 16, v217
	v_and_b32_e32 v13, 0xffff0000, v217
	v_lshlrev_b32_e32 v20, 16, v233
	v_and_b32_e32 v21, 0xffff0000, v233
	v_lshlrev_b32_e32 v14, 16, v218
	v_and_b32_e32 v15, 0xffff0000, v218
	v_lshlrev_b32_e32 v22, 16, v234
	v_and_b32_e32 v23, 0xffff0000, v234
	v_lshlrev_b32_e32 v16, 16, v219
	v_and_b32_e32 v17, 0xffff0000, v219
	v_lshlrev_b32_e32 v24, 16, v235
	v_and_b32_e32 v25, 0xffff0000, v235
	v_pk_mul_f32 v[26:27], v[134:135], s[40:41] op_sel_hi:[1,0]
	v_pk_mul_f32 v[28:29], v[136:137], s[40:41] op_sel_hi:[1,0]
	v_pk_mul_f32 v[30:31], v[130:131], s[40:41] op_sel_hi:[1,0]
	v_pk_mul_f32 v[32:33], v[132:133], s[40:41] op_sel_hi:[1,0]
	v_pk_fma_f32 v[26:27], v[26:27], v[10:11], v[18:19]
	v_pk_fma_f32 v[28:29], v[28:29], v[12:13], v[20:21]
	v_pk_fma_f32 v[30:31], v[30:31], v[14:15], v[22:23]
	v_pk_fma_f32 v[32:33], v[32:33], v[16:17], v[24:25]
	v_pk_mul_f32 v[26:27], v[26:27], s[84:85] op_sel_hi:[1,0]
	v_pk_mul_f32 v[28:29], v[28:29], s[84:85] op_sel_hi:[1,0]
	v_pk_mul_f32 v[30:31], v[30:31], s[84:85] op_sel_hi:[1,0]
	v_pk_mul_f32 v[32:33], v[32:33], s[84:85] op_sel_hi:[1,0]
	s_nop 0
	v_cvt_pk_fp8_f32 v248, v26, v27
	v_cvt_pk_fp8_f32 v249, v30, v31
	s_nop 0
	v_cvt_pk_fp8_f32 v248, v28, v29 op_sel:[0,0,1]
	v_cvt_pk_fp8_f32 v249, v32, v33 op_sel:[0,0,1]
	global_store_dwordx2 v[240:241], v[248:249], off offset:128
	global_load_dwordx4 v[216:219], v[236:237], off offset:256
	global_load_dwordx4 v[232:235], v[238:239], off offset:256
	v_add_u32_e32 v243, 0x20, v8
	v_lshlrev_b32_e32 v240, 11, v243
	v_mov_b32_e32 v241, 0
	v_lshl_add_u64 v[240:241], s[22:23], 0, v[240:241]
	v_lshl_add_u64 v[240:241], v[240:241], 0, v[2:3]
	s_waitcnt vmcnt(9)
	v_lshlrev_b32_e32 v10, 16, v204
	v_and_b32_e32 v11, 0xffff0000, v204
	v_lshlrev_b32_e32 v18, 16, v220
	v_and_b32_e32 v19, 0xffff0000, v220
	v_lshlrev_b32_e32 v12, 16, v205
	v_and_b32_e32 v13, 0xffff0000, v205
	v_lshlrev_b32_e32 v20, 16, v221
	v_and_b32_e32 v21, 0xffff0000, v221
	v_lshlrev_b32_e32 v14, 16, v206
	v_and_b32_e32 v15, 0xffff0000, v206
	v_lshlrev_b32_e32 v22, 16, v222
	v_and_b32_e32 v23, 0xffff0000, v222
	v_lshlrev_b32_e32 v16, 16, v207
	v_and_b32_e32 v17, 0xffff0000, v207
	v_lshlrev_b32_e32 v24, 16, v223
	v_and_b32_e32 v25, 0xffff0000, v223
	v_pk_mul_f32 v[26:27], v[126:127], s[40:41] op_sel_hi:[1,0]
	v_pk_mul_f32 v[28:29], v[128:129], s[40:41] op_sel_hi:[1,0]
	v_pk_mul_f32 v[30:31], v[122:123], s[40:41] op_sel_hi:[1,0]
	v_pk_mul_f32 v[32:33], v[124:125], s[40:41] op_sel_hi:[1,0]
	v_pk_fma_f32 v[26:27], v[26:27], v[10:11], v[18:19]
	v_pk_fma_f32 v[28:29], v[28:29], v[12:13], v[20:21]
	v_pk_fma_f32 v[30:31], v[30:31], v[14:15], v[22:23]
	v_pk_fma_f32 v[32:33], v[32:33], v[16:17], v[24:25]
	v_pk_mul_f32 v[26:27], v[26:27], s[84:85] op_sel_hi:[1,0]
	v_pk_mul_f32 v[28:29], v[28:29], s[84:85] op_sel_hi:[1,0]
	v_pk_mul_f32 v[30:31], v[30:31], s[84:85] op_sel_hi:[1,0]
	v_pk_mul_f32 v[32:33], v[32:33], s[84:85] op_sel_hi:[1,0]
	s_nop 0
	v_cvt_pk_fp8_f32 v244, v26, v27
	v_cvt_pk_fp8_f32 v245, v30, v31
	s_nop 0
	v_cvt_pk_fp8_f32 v244, v28, v29 op_sel:[0,0,1]
	v_cvt_pk_fp8_f32 v245, v32, v33 op_sel:[0,0,1]
	global_store_dwordx2 v[240:241], v[244:245], off
	v_add_u32_e32 v242, 0x80, v8
	v_mad_i64_i32 v[236:237], s[82:83], v242, s57, v[4:5]
	v_lshl_add_u64 v[236:237], v[236:237], 0, v[6:7]
	v_lshlrev_b32_e32 v238, 12, v242
	v_mov_b32_e32 v239, 0
	v_lshl_add_u64 v[238:239], s[8:9], 0, v[238:239]
	v_lshl_add_u64 v[238:239], v[238:239], 0, v[6:7]
	global_load_dwordx4 v[204:207], v[236:237], off
	global_load_dwordx4 v[220:223], v[238:239], off
	s_waitcnt vmcnt(9)
; __device__ __forceinline__ float bf_lo(unsigned w) { return __uint_as_float(w << 16); }
; __device__ __forceinline__ float bf_hi(unsigned w) { return __uint_as_float(w & 0xffff0000u); }
;     __device__ __forceinline__ void operator()(const f32x4 (&acc)[2][2][4][2], const Unit& u, int wr, int wc, int fr, int fq) const {
;         const int row0 = u.pm * BM + wr * 64 + fr; const int col0 = u.pn * BM + wc * 32 + 8 * fq;
; #pragma unroll
;         for (int ai = 0; ai < 2; ++ai)
; #pragma unroll
;             for (int m = 0; m < 4; ++m) { const size_t row = (size_t)(row0 + ai * HALF + m * 16);
; #pragma unroll
;                 for (int bj = 0; bj < 2; ++bj) { const int col = col0 + bj * HALF; const u32x4 g = *(const u32x4*)(G + row * ldg + col);
;                     const u32x4 mw = *(const u32x4*)(M1 + row * 2048 + col);
;                     const f32x4 m0 = {bf_lo(mw.x), bf_hi(mw.x), bf_lo(mw.y), bf_hi(mw.y)}, m1 = {bf_lo(mw.z), bf_hi(mw.z), bf_lo(mw.w), bf_hi(mw.w)};
;                     const f32x4 a0 = acc[ai][bj][m][0] * P5_ACC_SCALE, a1 = acc[ai][bj][m][1] * P5_ACC_SCALE;
;                     const f32x4 o0 = {m0[0] + a0[0] * bf_lo(g.x), m0[1] + a0[1] * bf_hi(g.x), m0[2] + a0[2] * bf_lo(g.y), m0[3] + a0[3] * bf_hi(g.y)};
;                     const f32x4 o1 = {m1[0] + a1[0] * bf_lo(g.z), m1[1] + a1[1] * bf_hi(g.z), m1[2] + a1[2] * bf_lo(g.w), m1[3] + a1[3] * bf_hi(g.w)};
;                     int w0 = __builtin_amdgcn_cvt_pk_fp8_f32(o0[0] * 16.f, o0[1] * 16.f, 0, false); w0 = __builtin_amdgcn_cvt_pk_fp8_f32(o0[2] * 16.f, o0[3] * 16.f, w0, true);
;                     int w1 = __builtin_amdgcn_cvt_pk_fp8_f32(o1[0] * 16.f, o1[1] * 16.f, 0, false); w1 = __builtin_amdgcn_cvt_pk_fp8_f32(o1[2] * 16.f, o1[3] * 16.f, w1, true);
;                     typedef int v2i_m __attribute__((ext_vector_type(2))); *(v2i_m*)(MG + row * 2048 + col) = (v2i_m){w0, w1}; } }
;     }
	v_lshlrev_b32_e32 v10, 16, v208
	v_and_b32_e32 v11, 0xffff0000, v208
	v_lshlrev_b32_e32 v18, 16, v224
	v_and_b32_e32 v19, 0xffff0000, v224
	v_lshlrev_b32_e32 v12, 16, v209
	v_and_b32_e32 v13, 0xffff0000, v209
	v_lshlrev_b32_e32 v20, 16, v225
	v_and_b32_e32 v21, 0xffff0000, v225
	v_lshlrev_b32_e32 v14, 16, v210
	v_and_b32_e32 v15, 0xffff0000, v210
	v_lshlrev_b32_e32 v22, 16, v226
	v_and_b32_e32 v23, 0xffff0000, v226
	v_lshlrev_b32_e32 v16, 16, v211
	v_and_b32_e32 v17, 0xffff0000, v211
	v_lshlrev_b32_e32 v24, 16, v227
	v_and_b32_e32 v25, 0xffff0000, v227
	v_pk_mul_f32 v[26:27], v[118:119], s[40:41] op_sel_hi:[1,0]
	v_pk_mul_f32 v[28:29], v[120:121], s[40:41] op_sel_hi:[1,0]
	v_pk_mul_f32 v[30:31], v[114:115], s[40:41] op_sel_hi:[1,0]
	v_pk_mul_f32 v[32:33], v[116:117], s[40:41] op_sel_hi:[1,0]
	v_pk_fma_f32 v[26:27], v[26:27], v[10:11], v[18:19]
	v_pk_fma_f32 v[28:29], v[28:29], v[12:13], v[20:21]
	v_pk_fma_f32 v[30:31], v[30:31], v[14:15], v[22:23]
	v_pk_fma_f32 v[32:33], v[32:33], v[16:17], v[24:25]
	v_pk_mul_f32 v[26:27], v[26:27], s[84:85] op_sel_hi:[1,0]
	v_pk_mul_f32 v[28:29], v[28:29], s[84:85] op_sel_hi:[1,0]
	v_pk_mul_f32 v[30:31], v[30:31], s[84:85] op_sel_hi:[1,0]
	v_pk_mul_f32 v[32:33], v[32:33], s[84:85] op_sel_hi:[1,0]
	s_nop 0
	v_cvt_pk_fp8_f32 v248, v26, v27
	v_cvt_pk_fp8_f32 v249, v30, v31
	s_nop 0
	v_cvt_pk_fp8_f32 v248, v28, v29 op_sel:[0,0,1]
	v_cvt_pk_fp8_f32 v249, v32, v33 op_sel:[0,0,1]
	global_store_dwordx2 v[240:241], v[248:249], off offset:128
	global_load_dwordx4 v[208:211], v[236:237], off offset:256
	global_load_dwordx4 v[224:227], v[238:239], off offset:256
	v_add_u32_e32 v243, 0x30, v8
	v_lshlrev_b32_e32 v240, 11, v243
	v_mov_b32_e32 v241, 0
	v_lshl_add_u64 v[240:241], s[22:23], 0, v[240:241]
	v_lshl_add_u64 v[240:241], v[240:241], 0, v[2:3]
	s_waitcnt vmcnt(9)
	v_lshlrev_b32_e32 v10, 16, v212
	v_and_b32_e32 v11, 0xffff0000, v212
	v_lshlrev_b32_e32 v18, 16, v228
	v_and_b32_e32 v19, 0xffff0000, v228
	v_lshlrev_b32_e32 v12, 16, v213
	v_and_b32_e32 v13, 0xffff0000, v213
	v_lshlrev_b32_e32 v20, 16, v229
	v_and_b32_e32 v21, 0xffff0000, v229
	v_lshlrev_b32_e32 v14, 16, v214
	v_and_b32_e32 v15, 0xffff0000, v214
	v_lshlrev_b32_e32 v22, 16, v230
	v_and_b32_e32 v23, 0xffff0000, v230
	v_lshlrev_b32_e32 v16, 16, v215
	v_and_b32_e32 v17, 0xffff0000, v215
	v_lshlrev_b32_e32 v24, 16, v231
	v_and_b32_e32 v25, 0xffff0000, v231
	v_pk_mul_f32 v[26:27], v[110:111], s[40:41] op_sel_hi:[1,0]
	v_pk_mul_f32 v[28:29], v[112:113], s[40:41] op_sel_hi:[1,0]
	v_pk_mul_f32 v[30:31], v[106:107], s[40:41] op_sel_hi:[1,0]
	v_pk_mul_f32 v[32:33], v[108:109], s[40:41] op_sel_hi:[1,0]
	v_pk_fma_f32 v[26:27], v[26:27], v[10:11], v[18:19]
	v_pk_fma_f32 v[28:29], v[28:29], v[12:13], v[20:21]
	v_pk_fma_f32 v[30:31], v[30:31], v[14:15], v[22:23]
	v_pk_fma_f32 v[32:33], v[32:33], v[16:17], v[24:25]
	v_pk_mul_f32 v[26:27], v[26:27], s[84:85] op_sel_hi:[1,0]
	v_pk_mul_f32 v[28:29], v[28:29], s[84:85] op_sel_hi:[1,0]
	v_pk_mul_f32 v[30:31], v[30:31], s[84:85] op_sel_hi:[1,0]
	v_pk_mul_f32 v[32:33], v[32:33], s[84:85] op_sel_hi:[1,0]
	s_nop 0
	v_cvt_pk_fp8_f32 v244, v26, v27
	v_cvt_pk_fp8_f32 v245, v30, v31
	s_nop 0
	v_cvt_pk_fp8_f32 v244, v28, v29 op_sel:[0,0,1]
	v_cvt_pk_fp8_f32 v245, v32, v33 op_sel:[0,0,1]
	global_store_dwordx2 v[240:241], v[244:245], off
	v_add_u32_e32 v242, 0x90, v8
	v_mad_i64_i32 v[236:237], s[82:83], v242, s57, v[4:5]
	v_lshl_add_u64 v[236:237], v[236:237], 0, v[6:7]
	v_lshlrev_b32_e32 v238, 12, v242
	v_mov_b32_e32 v239, 0
	v_lshl_add_u64 v[238:239], s[8:9], 0, v[238:239]
	v_lshl_add_u64 v[238:239], v[238:239], 0, v[6:7]
	global_load_dwordx4 v[212:215], v[236:237], off
	global_load_dwordx4 v[228:231], v[238:239], off
	s_waitcnt vmcnt(9)
	v_lshlrev_b32_e32 v10, 16, v216
	v_and_b32_e32 v11, 0xffff0000, v216
	v_lshlrev_b32_e32 v18, 16, v232
	v_and_b32_e32 v19, 0xffff0000, v232
	v_lshlrev_b32_e32 v12, 16, v217
	v_and_b32_e32 v13, 0xffff0000, v217
	v_lshlrev_b32_e32 v20, 16, v233
	v_and_b32_e32 v21, 0xffff0000, v233
	v_lshlrev_b32_e32 v14, 16, v218
	v_and_b32_e32 v15, 0xffff0000, v218
	v_lshlrev_b32_e32 v22, 16, v234
	v_and_b32_e32 v23, 0xffff0000, v234
	v_lshlrev_b32_e32 v16, 16, v219
	v_and_b32_e32 v17, 0xffff0000, v219
	v_lshlrev_b32_e32 v24, 16, v235
	v_and_b32_e32 v25, 0xffff0000, v235
	v_pk_mul_f32 v[26:27], v[102:103], s[40:41] op_sel_hi:[1,0]
	v_pk_mul_f32 v[28:29], v[104:105], s[40:41] op_sel_hi:[1,0]
	v_pk_mul_f32 v[30:31], v[98:99], s[40:41] op_sel_hi:[1,0]
	v_pk_mul_f32 v[32:33], v[100:101], s[40:41] op_sel_hi:[1,0]
	v_pk_fma_f32 v[26:27], v[26:27], v[10:11], v[18:19]
	v_pk_fma_f32 v[28:29], v[28:29], v[12:13], v[20:21]
	v_pk_fma_f32 v[30:31], v[30:31], v[14:15], v[22:23]
	v_pk_fma_f32 v[32:33], v[32:33], v[16:17], v[24:25]
	v_pk_mul_f32 v[26:27], v[26:27], s[84:85] op_sel_hi:[1,0]
	v_pk_mul_f32 v[28:29], v[28:29], s[84:85] op_sel_hi:[1,0]
	v_pk_mul_f32 v[30:31], v[30:31], s[84:85] op_sel_hi:[1,0]
	v_pk_mul_f32 v[32:33], v[32:33], s[84:85] op_sel_hi:[1,0]
	s_nop 0
	v_cvt_pk_fp8_f32 v248, v26, v27
	v_cvt_pk_fp8_f32 v249, v30, v31
	s_nop 0
	v_cvt_pk_fp8_f32 v248, v28, v29 op_sel:[0,0,1]
	v_cvt_pk_fp8_f32 v249, v32, v33 op_sel:[0,0,1]
	global_store_dwordx2 v[240:241], v[248:249], off offset:128
	global_load_dwordx4 v[216:219], v[236:237], off offset:256
	global_load_dwordx4 v[232:235], v[238:239], off offset:256
	v_add_u32_e32 v243, 0x80, v8
	v_lshlrev_b32_e32 v240, 11, v243
	v_mov_b32_e32 v241, 0
	v_lshl_add_u64 v[240:241], s[22:23], 0, v[240:241]
	v_lshl_add_u64 v[240:241], v[240:241], 0, v[2:3]
	s_waitcnt vmcnt(9)
; __device__ __forceinline__ float bf_lo(unsigned w) { return __uint_as_float(w << 16); }
; __device__ __forceinline__ float bf_hi(unsigned w) { return __uint_as_float(w & 0xffff0000u); }
;     __device__ __forceinline__ void operator()(const f32x4 (&acc)[2][2][4][2], const Unit& u, int wr, int wc, int fr, int fq) const {
;         const int row0 = u.pm * BM + wr * 64 + fr; const int col0 = u.pn * BM + wc * 32 + 8 * fq;
; #pragma unroll
;         for (int ai = 0; ai < 2; ++ai)
; #pragma unroll
;             for (int m = 0; m < 4; ++m) { const size_t row = (size_t)(row0 + ai * HALF + m * 16);
; #pragma unroll
;                 for (int bj = 0; bj < 2; ++bj) { const int col = col0 + bj * HALF; const u32x4 g = *(const u32x4*)(G + row * ldg + col);
;                     const u32x4 mw = *(const u32x4*)(M1 + row * 2048 + col);
;                     const f32x4 m0 = {bf_lo(mw.x), bf_hi(mw.x), bf_lo(mw.y), bf_hi(mw.y)}, m1 = {bf_lo(mw.z), bf_hi(mw.z), bf_lo(mw.w), bf_hi(mw.w)};
;                     const f32x4 a0 = acc[ai][bj][m][0] * P5_ACC_SCALE, a1 = acc[ai][bj][m][1] * P5_ACC_SCALE;
;                     const f32x4 o0 = {m0[0] + a0[0] * bf_lo(g.x), m0[1] + a0[1] * bf_hi(g.x), m0[2] + a0[2] * bf_lo(g.y), m0[3] + a0[3] * bf_hi(g.y)};
;                     const f32x4 o1 = {m1[0] + a1[0] * bf_lo(g.z), m1[1] + a1[1] * bf_hi(g.z), m1[2] + a1[2] * bf_lo(g.w), m1[3] + a1[3] * bf_hi(g.w)};
;                     int w0 = __builtin_amdgcn_cvt_pk_fp8_f32(o0[0] * 16.f, o0[1] * 16.f, 0, false); w0 = __builtin_amdgcn_cvt_pk_fp8_f32(o0[2] * 16.f, o0[3] * 16.f, w0, true);
;                     int w1 = __builtin_amdgcn_cvt_pk_fp8_f32(o1[0] * 16.f, o1[1] * 16.f, 0, false); w1 = __builtin_amdgcn_cvt_pk_fp8_f32(o1[2] * 16.f, o1[3] * 16.f, w1, true);
;                     typedef int v2i_m __attribute__((ext_vector_type(2))); *(v2i_m*)(MG + row * 2048 + col) = (v2i_m){w0, w1}; } }
;     }
	v_lshlrev_b32_e32 v10, 16, v204
	v_and_b32_e32 v11, 0xffff0000, v204
	v_lshlrev_b32_e32 v18, 16, v220
	v_and_b32_e32 v19, 0xffff0000, v220
	v_lshlrev_b32_e32 v12, 16, v205
	v_and_b32_e32 v13, 0xffff0000, v205
	v_lshlrev_b32_e32 v20, 16, v221
	v_and_b32_e32 v21, 0xffff0000, v221
	v_lshlrev_b32_e32 v14, 16, v206
	v_and_b32_e32 v15, 0xffff0000, v206
	v_lshlrev_b32_e32 v22, 16, v222
	v_and_b32_e32 v23, 0xffff0000, v222
	v_lshlrev_b32_e32 v16, 16, v207
	v_and_b32_e32 v17, 0xffff0000, v207
	v_lshlrev_b32_e32 v24, 16, v223
	v_and_b32_e32 v25, 0xffff0000, v223
	v_pk_mul_f32 v[26:27], v[94:95], s[40:41] op_sel_hi:[1,0]
	v_pk_mul_f32 v[28:29], v[96:97], s[40:41] op_sel_hi:[1,0]
	v_pk_mul_f32 v[30:31], v[90:91], s[40:41] op_sel_hi:[1,0]
	v_pk_mul_f32 v[32:33], v[92:93], s[40:41] op_sel_hi:[1,0]
	v_pk_fma_f32 v[26:27], v[26:27], v[10:11], v[18:19]
	v_pk_fma_f32 v[28:29], v[28:29], v[12:13], v[20:21]
	v_pk_fma_f32 v[30:31], v[30:31], v[14:15], v[22:23]
	v_pk_fma_f32 v[32:33], v[32:33], v[16:17], v[24:25]
	v_pk_mul_f32 v[26:27], v[26:27], s[84:85] op_sel_hi:[1,0]
	v_pk_mul_f32 v[28:29], v[28:29], s[84:85] op_sel_hi:[1,0]
	v_pk_mul_f32 v[30:31], v[30:31], s[84:85] op_sel_hi:[1,0]
	v_pk_mul_f32 v[32:33], v[32:33], s[84:85] op_sel_hi:[1,0]
	s_nop 0
	v_cvt_pk_fp8_f32 v244, v26, v27
	v_cvt_pk_fp8_f32 v245, v30, v31
	s_nop 0
	v_cvt_pk_fp8_f32 v244, v28, v29 op_sel:[0,0,1]
	v_cvt_pk_fp8_f32 v245, v32, v33 op_sel:[0,0,1]
	global_store_dwordx2 v[240:241], v[244:245], off
	v_add_u32_e32 v242, 0xa0, v8
	v_mad_i64_i32 v[236:237], s[82:83], v242, s57, v[4:5]
	v_lshl_add_u64 v[236:237], v[236:237], 0, v[6:7]
	v_lshlrev_b32_e32 v238, 12, v242
	v_mov_b32_e32 v239, 0
	v_lshl_add_u64 v[238:239], s[8:9], 0, v[238:239]
	v_lshl_add_u64 v[238:239], v[238:239], 0, v[6:7]
	global_load_dwordx4 v[204:207], v[236:237], off
	global_load_dwordx4 v[220:223], v[238:239], off
	s_waitcnt vmcnt(9)
	v_lshlrev_b32_e32 v10, 16, v208
	v_and_b32_e32 v11, 0xffff0000, v208
	v_lshlrev_b32_e32 v18, 16, v224
	v_and_b32_e32 v19, 0xffff0000, v224
	v_lshlrev_b32_e32 v12, 16, v209
	v_and_b32_e32 v13, 0xffff0000, v209
	v_lshlrev_b32_e32 v20, 16, v225
	v_and_b32_e32 v21, 0xffff0000, v225
	v_lshlrev_b32_e32 v14, 16, v210
	v_and_b32_e32 v15, 0xffff0000, v210
	v_lshlrev_b32_e32 v22, 16, v226
	v_and_b32_e32 v23, 0xffff0000, v226
	v_lshlrev_b32_e32 v16, 16, v211
	v_and_b32_e32 v17, 0xffff0000, v211
	v_lshlrev_b32_e32 v24, 16, v227
	v_and_b32_e32 v25, 0xffff0000, v227
	v_pk_mul_f32 v[26:27], v[86:87], s[40:41] op_sel_hi:[1,0]
	v_pk_mul_f32 v[28:29], v[88:89], s[40:41] op_sel_hi:[1,0]
	v_pk_mul_f32 v[30:31], v[82:83], s[40:41] op_sel_hi:[1,0]
	v_pk_mul_f32 v[32:33], v[84:85], s[40:41] op_sel_hi:[1,0]
	v_pk_fma_f32 v[26:27], v[26:27], v[10:11], v[18:19]
	v_pk_fma_f32 v[28:29], v[28:29], v[12:13], v[20:21]
	v_pk_fma_f32 v[30:31], v[30:31], v[14:15], v[22:23]
	v_pk_fma_f32 v[32:33], v[32:33], v[16:17], v[24:25]
	v_pk_mul_f32 v[26:27], v[26:27], s[84:85] op_sel_hi:[1,0]
	v_pk_mul_f32 v[28:29], v[28:29], s[84:85] op_sel_hi:[1,0]
	v_pk_mul_f32 v[30:31], v[30:31], s[84:85] op_sel_hi:[1,0]
	v_pk_mul_f32 v[32:33], v[32:33], s[84:85] op_sel_hi:[1,0]
	s_nop 0
	v_cvt_pk_fp8_f32 v248, v26, v27
	v_cvt_pk_fp8_f32 v249, v30, v31
	s_nop 0
	v_cvt_pk_fp8_f32 v248, v28, v29 op_sel:[0,0,1]
	v_cvt_pk_fp8_f32 v249, v32, v33 op_sel:[0,0,1]
	global_store_dwordx2 v[240:241], v[248:249], off offset:128
	global_load_dwordx4 v[208:211], v[236:237], off offset:256
	global_load_dwordx4 v[224:227], v[238:239], off offset:256
	v_add_u32_e32 v243, 0x90, v8
	v_lshlrev_b32_e32 v240, 11, v243
	v_mov_b32_e32 v241, 0
	v_lshl_add_u64 v[240:241], s[22:23], 0, v[240:241]
	v_lshl_add_u64 v[240:241], v[240:241], 0, v[2:3]
	s_waitcnt vmcnt(9)
	v_lshlrev_b32_e32 v10, 16, v212
	v_and_b32_e32 v11, 0xffff0000, v212
	v_lshlrev_b32_e32 v18, 16, v228
	v_and_b32_e32 v19, 0xffff0000, v228
	v_lshlrev_b32_e32 v12, 16, v213
	v_and_b32_e32 v13, 0xffff0000, v213
	v_lshlrev_b32_e32 v20, 16, v229
	v_and_b32_e32 v21, 0xffff0000, v229
	v_lshlrev_b32_e32 v14, 16, v214
	v_and_b32_e32 v15, 0xffff0000, v214
	v_lshlrev_b32_e32 v22, 16, v230
	v_and_b32_e32 v23, 0xffff0000, v230
	v_lshlrev_b32_e32 v16, 16, v215
	v_and_b32_e32 v17, 0xffff0000, v215
	v_lshlrev_b32_e32 v24, 16, v231
	v_and_b32_e32 v25, 0xffff0000, v231
	v_pk_mul_f32 v[26:27], v[78:79], s[40:41] op_sel_hi:[1,0]
	v_pk_mul_f32 v[28:29], v[80:81], s[40:41] op_sel_hi:[1,0]
	v_pk_mul_f32 v[30:31], v[74:75], s[40:41] op_sel_hi:[1,0]
	v_pk_mul_f32 v[32:33], v[76:77], s[40:41] op_sel_hi:[1,0]
	v_pk_fma_f32 v[26:27], v[26:27], v[10:11], v[18:19]
	v_pk_fma_f32 v[28:29], v[28:29], v[12:13], v[20:21]
	v_pk_fma_f32 v[30:31], v[30:31], v[14:15], v[22:23]
	v_pk_fma_f32 v[32:33], v[32:33], v[16:17], v[24:25]
	v_pk_mul_f32 v[26:27], v[26:27], s[84:85] op_sel_hi:[1,0]
	v_pk_mul_f32 v[28:29], v[28:29], s[84:85] op_sel_hi:[1,0]
	v_pk_mul_f32 v[30:31], v[30:31], s[84:85] op_sel_hi:[1,0]
	v_pk_mul_f32 v[32:33], v[32:33], s[84:85] op_sel_hi:[1,0]
	s_nop 0
	v_cvt_pk_fp8_f32 v244, v26, v27
	v_cvt_pk_fp8_f32 v245, v30, v31
	s_nop 0
	v_cvt_pk_fp8_f32 v244, v28, v29 op_sel:[0,0,1]
	v_cvt_pk_fp8_f32 v245, v32, v33 op_sel:[0,0,1]
	global_store_dwordx2 v[240:241], v[244:245], off
	v_add_u32_e32 v242, 0xb0, v8
	v_mad_i64_i32 v[236:237], s[82:83], v242, s57, v[4:5]
	v_lshl_add_u64 v[236:237], v[236:237], 0, v[6:7]
	v_lshlrev_b32_e32 v238, 12, v242
	v_mov_b32_e32 v239, 0
	v_lshl_add_u64 v[238:239], s[8:9], 0, v[238:239]
	v_lshl_add_u64 v[238:239], v[238:239], 0, v[6:7]
	global_load_dwordx4 v[212:215], v[236:237], off
	global_load_dwordx4 v[228:231], v[238:239], off
	s_waitcnt vmcnt(9)
; __device__ __forceinline__ float bf_lo(unsigned w) { return __uint_as_float(w << 16); }
; __device__ __forceinline__ float bf_hi(unsigned w) { return __uint_as_float(w & 0xffff0000u); }
;     __device__ __forceinline__ void operator()(const f32x4 (&acc)[2][2][4][2], const Unit& u, int wr, int wc, int fr, int fq) const {
;         const int row0 = u.pm * BM + wr * 64 + fr; const int col0 = u.pn * BM + wc * 32 + 8 * fq;
; #pragma unroll
;         for (int ai = 0; ai < 2; ++ai)
; #pragma unroll
;             for (int m = 0; m < 4; ++m) { const size_t row = (size_t)(row0 + ai * HALF + m * 16);
; #pragma unroll
;                 for (int bj = 0; bj < 2; ++bj) { const int col = col0 + bj * HALF; const u32x4 g = *(const u32x4*)(G + row * ldg + col);
;                     const u32x4 mw = *(const u32x4*)(M1 + row * 2048 + col);
;                     const f32x4 m0 = {bf_lo(mw.x), bf_hi(mw.x), bf_lo(mw.y), bf_hi(mw.y)}, m1 = {bf_lo(mw.z), bf_hi(mw.z), bf_lo(mw.w), bf_hi(mw.w)};
;                     const f32x4 a0 = acc[ai][bj][m][0] * P5_ACC_SCALE, a1 = acc[ai][bj][m][1] * P5_ACC_SCALE;
;                     const f32x4 o0 = {m0[0] + a0[0] * bf_lo(g.x), m0[1] + a0[1] * bf_hi(g.x), m0[2] + a0[2] * bf_lo(g.y), m0[3] + a0[3] * bf_hi(g.y)};
;                     const f32x4 o1 = {m1[0] + a1[0] * bf_lo(g.z), m1[1] + a1[1] * bf_hi(g.z), m1[2] + a1[2] * bf_lo(g.w), m1[3] + a1[3] * bf_hi(g.w)};
;                     int w0 = __builtin_amdgcn_cvt_pk_fp8_f32(o0[0] * 16.f, o0[1] * 16.f, 0, false); w0 = __builtin_amdgcn_cvt_pk_fp8_f32(o0[2] * 16.f, o0[3] * 16.f, w0, true);
;                     int w1 = __builtin_amdgcn_cvt_pk_fp8_f32(o1[0] * 16.f, o1[1] * 16.f, 0, false); w1 = __builtin_amdgcn_cvt_pk_fp8_f32(o1[2] * 16.f, o1[3] * 16.f, w1, true);
;                     typedef int v2i_m __attribute__((ext_vector_type(2))); *(v2i_m*)(MG + row * 2048 + col) = (v2i_m){w0, w1}; } }
;     }
	v_lshlrev_b32_e32 v10, 16, v216
	v_and_b32_e32 v11, 0xffff0000, v216
	v_lshlrev_b32_e32 v18, 16, v232
	v_and_b32_e32 v19, 0xffff0000, v232
	v_lshlrev_b32_e32 v12, 16, v217
	v_and_b32_e32 v13, 0xffff0000, v217
	v_lshlrev_b32_e32 v20, 16, v233
	v_and_b32_e32 v21, 0xffff0000, v233
	v_lshlrev_b32_e32 v14, 16, v218
	v_and_b32_e32 v15, 0xffff0000, v218
	v_lshlrev_b32_e32 v22, 16, v234
	v_and_b32_e32 v23, 0xffff0000, v234
	v_lshlrev_b32_e32 v16, 16, v219
	v_and_b32_e32 v17, 0xffff0000, v219
	v_lshlrev_b32_e32 v24, 16, v235
	v_and_b32_e32 v25, 0xffff0000, v235
	v_pk_mul_f32 v[26:27], v[70:71], s[40:41] op_sel_hi:[1,0]
	v_pk_mul_f32 v[28:29], v[72:73], s[40:41] op_sel_hi:[1,0]
	v_pk_mul_f32 v[30:31], v[66:67], s[40:41] op_sel_hi:[1,0]
	v_pk_mul_f32 v[32:33], v[68:69], s[40:41] op_sel_hi:[1,0]
	v_pk_fma_f32 v[26:27], v[26:27], v[10:11], v[18:19]
	v_pk_fma_f32 v[28:29], v[28:29], v[12:13], v[20:21]
	v_pk_fma_f32 v[30:31], v[30:31], v[14:15], v[22:23]
	v_pk_fma_f32 v[32:33], v[32:33], v[16:17], v[24:25]
	v_pk_mul_f32 v[26:27], v[26:27], s[84:85] op_sel_hi:[1,0]
	v_pk_mul_f32 v[28:29], v[28:29], s[84:85] op_sel_hi:[1,0]
	v_pk_mul_f32 v[30:31], v[30:31], s[84:85] op_sel_hi:[1,0]
	v_pk_mul_f32 v[32:33], v[32:33], s[84:85] op_sel_hi:[1,0]
	s_nop 0
	v_cvt_pk_fp8_f32 v248, v26, v27
	v_cvt_pk_fp8_f32 v249, v30, v31
	s_nop 0
	v_cvt_pk_fp8_f32 v248, v28, v29 op_sel:[0,0,1]
	v_cvt_pk_fp8_f32 v249, v32, v33 op_sel:[0,0,1]
	global_store_dwordx2 v[240:241], v[248:249], off offset:128
	global_load_dwordx4 v[216:219], v[236:237], off offset:256
	global_load_dwordx4 v[232:235], v[238:239], off offset:256
	v_add_u32_e32 v243, 0xa0, v8
	v_lshlrev_b32_e32 v240, 11, v243
	v_mov_b32_e32 v241, 0
	v_lshl_add_u64 v[240:241], s[22:23], 0, v[240:241]
	v_lshl_add_u64 v[240:241], v[240:241], 0, v[2:3]
	s_waitcnt vmcnt(9)
	v_lshlrev_b32_e32 v10, 16, v204
	v_and_b32_e32 v11, 0xffff0000, v204
	v_lshlrev_b32_e32 v18, 16, v220
	v_and_b32_e32 v19, 0xffff0000, v220
	v_lshlrev_b32_e32 v12, 16, v205
	v_and_b32_e32 v13, 0xffff0000, v205
	v_lshlrev_b32_e32 v20, 16, v221
	v_and_b32_e32 v21, 0xffff0000, v221
	v_lshlrev_b32_e32 v14, 16, v206
	v_and_b32_e32 v15, 0xffff0000, v206
	v_lshlrev_b32_e32 v22, 16, v222
	v_and_b32_e32 v23, 0xffff0000, v222
	v_lshlrev_b32_e32 v16, 16, v207
	v_and_b32_e32 v17, 0xffff0000, v207
	v_lshlrev_b32_e32 v24, 16, v223
	v_and_b32_e32 v25, 0xffff0000, v223
	v_pk_mul_f32 v[26:27], v[62:63], s[40:41] op_sel_hi:[1,0]
	v_pk_mul_f32 v[28:29], v[64:65], s[40:41] op_sel_hi:[1,0]
	v_pk_mul_f32 v[30:31], v[58:59], s[40:41] op_sel_hi:[1,0]
	v_pk_mul_f32 v[32:33], v[60:61], s[40:41] op_sel_hi:[1,0]
	v_pk_fma_f32 v[26:27], v[26:27], v[10:11], v[18:19]
	v_pk_fma_f32 v[28:29], v[28:29], v[12:13], v[20:21]
	v_pk_fma_f32 v[30:31], v[30:31], v[14:15], v[22:23]
	v_pk_fma_f32 v[32:33], v[32:33], v[16:17], v[24:25]
	v_pk_mul_f32 v[26:27], v[26:27], s[84:85] op_sel_hi:[1,0]
	v_pk_mul_f32 v[28:29], v[28:29], s[84:85] op_sel_hi:[1,0]
	v_pk_mul_f32 v[30:31], v[30:31], s[84:85] op_sel_hi:[1,0]
	v_pk_mul_f32 v[32:33], v[32:33], s[84:85] op_sel_hi:[1,0]
	s_nop 0
	v_cvt_pk_fp8_f32 v244, v26, v27
	v_cvt_pk_fp8_f32 v245, v30, v31
	s_nop 0
	v_cvt_pk_fp8_f32 v244, v28, v29 op_sel:[0,0,1]
	v_cvt_pk_fp8_f32 v245, v32, v33 op_sel:[0,0,1]
	global_store_dwordx2 v[240:241], v[244:245], off
	s_waitcnt vmcnt(7)
; __device__ __forceinline__ float bf_lo(unsigned w) { return __uint_as_float(w << 16); }
; __device__ __forceinline__ float bf_hi(unsigned w) { return __uint_as_float(w & 0xffff0000u); }
;     __device__ __forceinline__ void operator()(const f32x4 (&acc)[2][2][4][2], const Unit& u, int wr, int wc, int fr, int fq) const {
;         const int row0 = u.pm * BM + wr * 64 + fr; const int col0 = u.pn * BM + wc * 32 + 8 * fq;
; #pragma unroll
;         for (int ai = 0; ai < 2; ++ai)
; #pragma unroll
;             for (int m = 0; m < 4; ++m) { const size_t row = (size_t)(row0 + ai * HALF + m * 16);
; #pragma unroll
;                 for (int bj = 0; bj < 2; ++bj) { const int col = col0 + bj * HALF; const u32x4 g = *(const u32x4*)(G + row * ldg + col);
;                     const u32x4 mw = *(const u32x4*)(M1 + row * 2048 + col);
;                     const f32x4 m0 = {bf_lo(mw.x), bf_hi(mw.x), bf_lo(mw.y), bf_hi(mw.y)}, m1 = {bf_lo(mw.z), bf_hi(mw.z), bf_lo(mw.w), bf_hi(mw.w)};
;                     const f32x4 a0 = acc[ai][bj][m][0] * P5_ACC_SCALE, a1 = acc[ai][bj][m][1] * P5_ACC_SCALE;
;                     const f32x4 o0 = {m0[0] + a0[0] * bf_lo(g.x), m0[1] + a0[1] * bf_hi(g.x), m0[2] + a0[2] * bf_lo(g.y), m0[3] + a0[3] * bf_hi(g.y)};
;                     const f32x4 o1 = {m1[0] + a1[0] * bf_lo(g.z), m1[1] + a1[1] * bf_hi(g.z), m1[2] + a1[2] * bf_lo(g.w), m1[3] + a1[3] * bf_hi(g.w)};
;                     int w0 = __builtin_amdgcn_cvt_pk_fp8_f32(o0[0] * 16.f, o0[1] * 16.f, 0, false); w0 = __builtin_amdgcn_cvt_pk_fp8_f32(o0[2] * 16.f, o0[3] * 16.f, w0, true);
;                     int w1 = __builtin_amdgcn_cvt_pk_fp8_f32(o1[0] * 16.f, o1[1] * 16.f, 0, false); w1 = __builtin_amdgcn_cvt_pk_fp8_f32(o1[2] * 16.f, o1[3] * 16.f, w1, true);
;                     typedef int v2i_m __attribute__((ext_vector_type(2))); *(v2i_m*)(MG + row * 2048 + col) = (v2i_m){w0, w1}; } }
;     }
	v_lshlrev_b32_e32 v10, 16, v208
	v_and_b32_e32 v11, 0xffff0000, v208
	v_lshlrev_b32_e32 v18, 16, v224
	v_and_b32_e32 v19, 0xffff0000, v224
	v_lshlrev_b32_e32 v12, 16, v209
	v_and_b32_e32 v13, 0xffff0000, v209
	v_lshlrev_b32_e32 v20, 16, v225
	v_and_b32_e32 v21, 0xffff0000, v225
	v_lshlrev_b32_e32 v14, 16, v210
	v_and_b32_e32 v15, 0xffff0000, v210
	v_lshlrev_b32_e32 v22, 16, v226
	v_and_b32_e32 v23, 0xffff0000, v226
	v_lshlrev_b32_e32 v16, 16, v211
	v_and_b32_e32 v17, 0xffff0000, v211
	v_lshlrev_b32_e32 v24, 16, v227
	v_and_b32_e32 v25, 0xffff0000, v227
	v_pk_mul_f32 v[26:27], v[54:55], s[40:41] op_sel_hi:[1,0]
	v_pk_mul_f32 v[28:29], v[56:57], s[40:41] op_sel_hi:[1,0]
	v_pk_mul_f32 v[30:31], v[50:51], s[40:41] op_sel_hi:[1,0]
	v_pk_mul_f32 v[32:33], v[52:53], s[40:41] op_sel_hi:[1,0]
	v_pk_fma_f32 v[26:27], v[26:27], v[10:11], v[18:19]
	v_pk_fma_f32 v[28:29], v[28:29], v[12:13], v[20:21]
	v_pk_fma_f32 v[30:31], v[30:31], v[14:15], v[22:23]
	v_pk_fma_f32 v[32:33], v[32:33], v[16:17], v[24:25]
	v_pk_mul_f32 v[26:27], v[26:27], s[84:85] op_sel_hi:[1,0]
	v_pk_mul_f32 v[28:29], v[28:29], s[84:85] op_sel_hi:[1,0]
	v_pk_mul_f32 v[30:31], v[30:31], s[84:85] op_sel_hi:[1,0]
	v_pk_mul_f32 v[32:33], v[32:33], s[84:85] op_sel_hi:[1,0]
	s_nop 0
	v_cvt_pk_fp8_f32 v248, v26, v27
	v_cvt_pk_fp8_f32 v249, v30, v31
	s_nop 0
	v_cvt_pk_fp8_f32 v248, v28, v29 op_sel:[0,0,1]
	v_cvt_pk_fp8_f32 v249, v32, v33 op_sel:[0,0,1]
	global_store_dwordx2 v[240:241], v[248:249], off offset:128
	v_add_u32_e32 v243, 0xb0, v8
	v_lshlrev_b32_e32 v240, 11, v243
	v_mov_b32_e32 v241, 0
	v_lshl_add_u64 v[240:241], s[22:23], 0, v[240:241]
	v_lshl_add_u64 v[240:241], v[240:241], 0, v[2:3]
	s_waitcnt vmcnt(5)
	v_lshlrev_b32_e32 v10, 16, v212
	v_and_b32_e32 v11, 0xffff0000, v212
	v_lshlrev_b32_e32 v18, 16, v228
	v_and_b32_e32 v19, 0xffff0000, v228
	v_lshlrev_b32_e32 v12, 16, v213
	v_and_b32_e32 v13, 0xffff0000, v213
	v_lshlrev_b32_e32 v20, 16, v229
	v_and_b32_e32 v21, 0xffff0000, v229
	v_lshlrev_b32_e32 v14, 16, v214
	v_and_b32_e32 v15, 0xffff0000, v214
	v_lshlrev_b32_e32 v22, 16, v230
	v_and_b32_e32 v23, 0xffff0000, v230
	v_lshlrev_b32_e32 v16, 16, v215
	v_and_b32_e32 v17, 0xffff0000, v215
	v_lshlrev_b32_e32 v24, 16, v231
	v_and_b32_e32 v25, 0xffff0000, v231
	v_pk_mul_f32 v[26:27], v[46:47], s[40:41] op_sel_hi:[1,0]
	v_pk_mul_f32 v[28:29], v[48:49], s[40:41] op_sel_hi:[1,0]
	v_pk_mul_f32 v[30:31], v[42:43], s[40:41] op_sel_hi:[1,0]
	v_pk_mul_f32 v[32:33], v[44:45], s[40:41] op_sel_hi:[1,0]
	v_pk_fma_f32 v[26:27], v[26:27], v[10:11], v[18:19]
	v_pk_fma_f32 v[28:29], v[28:29], v[12:13], v[20:21]
	v_pk_fma_f32 v[30:31], v[30:31], v[14:15], v[22:23]
	v_pk_fma_f32 v[32:33], v[32:33], v[16:17], v[24:25]
	v_pk_mul_f32 v[26:27], v[26:27], s[84:85] op_sel_hi:[1,0]
	v_pk_mul_f32 v[28:29], v[28:29], s[84:85] op_sel_hi:[1,0]
	v_pk_mul_f32 v[30:31], v[30:31], s[84:85] op_sel_hi:[1,0]
	v_pk_mul_f32 v[32:33], v[32:33], s[84:85] op_sel_hi:[1,0]
	s_nop 0
	v_cvt_pk_fp8_f32 v244, v26, v27
	v_cvt_pk_fp8_f32 v245, v30, v31
	s_nop 0
	v_cvt_pk_fp8_f32 v244, v28, v29 op_sel:[0,0,1]
	v_cvt_pk_fp8_f32 v245, v32, v33 op_sel:[0,0,1]
	global_store_dwordx2 v[240:241], v[244:245], off
	s_waitcnt vmcnt(3)
	v_lshlrev_b32_e32 v10, 16, v216
	v_and_b32_e32 v11, 0xffff0000, v216
	v_lshlrev_b32_e32 v18, 16, v232
	v_and_b32_e32 v19, 0xffff0000, v232
	v_lshlrev_b32_e32 v12, 16, v217
	v_and_b32_e32 v13, 0xffff0000, v217
	v_lshlrev_b32_e32 v20, 16, v233
	v_and_b32_e32 v21, 0xffff0000, v233
	v_lshlrev_b32_e32 v14, 16, v218
	v_and_b32_e32 v15, 0xffff0000, v218
	v_lshlrev_b32_e32 v22, 16, v234
	v_and_b32_e32 v23, 0xffff0000, v234
	v_lshlrev_b32_e32 v16, 16, v219
	v_and_b32_e32 v17, 0xffff0000, v219
	v_lshlrev_b32_e32 v24, 16, v235
	v_and_b32_e32 v25, 0xffff0000, v235
	v_pk_mul_f32 v[26:27], v[38:39], s[40:41] op_sel_hi:[1,0]
	v_pk_mul_f32 v[28:29], v[40:41], s[40:41] op_sel_hi:[1,0]
	v_pk_mul_f32 v[30:31], v[34:35], s[40:41] op_sel_hi:[1,0]
	v_pk_mul_f32 v[32:33], v[36:37], s[40:41] op_sel_hi:[1,0]
	v_pk_fma_f32 v[26:27], v[26:27], v[10:11], v[18:19]
	v_pk_fma_f32 v[28:29], v[28:29], v[12:13], v[20:21]
	v_pk_fma_f32 v[30:31], v[30:31], v[14:15], v[22:23]
	v_pk_fma_f32 v[32:33], v[32:33], v[16:17], v[24:25]
	v_pk_mul_f32 v[26:27], v[26:27], s[84:85] op_sel_hi:[1,0]
	v_pk_mul_f32 v[28:29], v[28:29], s[84:85] op_sel_hi:[1,0]
	v_pk_mul_f32 v[30:31], v[30:31], s[84:85] op_sel_hi:[1,0]
	v_pk_mul_f32 v[32:33], v[32:33], s[84:85] op_sel_hi:[1,0]
	s_nop 0
	v_cvt_pk_fp8_f32 v248, v26, v27
	v_cvt_pk_fp8_f32 v249, v30, v31
	s_nop 0
	v_cvt_pk_fp8_f32 v248, v28, v29 op_sel:[0,0,1]
	v_cvt_pk_fp8_f32 v249, v32, v33 op_sel:[0,0,1]
	global_store_dwordx2 v[240:241], v[248:249], off offset:128
	s_cbranch_vccnz .LBB0_742
	s_andn2_b64 vcc, exec, s[14:15]
	s_cbranch_vccnz .LBB0_741
	s_barrier
	s_branch .LBB0_741
